# speedup vs baseline: 1.0308x; 1.0308x over previous
.LBB1_4:
	s_or_b64 exec, exec, s[2:3]
	s_mul_i32 s2, s22, 27
	s_mul_i32 s3, s26, 9
	s_and_b32 s27, s10, 63
	s_add_i32 s2, s2, s3
	s_mov_b32 s3, 0
	s_sub_i32 s13, s27, s12
	s_lshl_b64 s[10:11], s[2:3], 14
	s_waitcnt lgkmcnt(0)
	s_add_u32 s6, s6, s10
	s_addc_u32 s7, s7, s11
	s_mov_b32 s23, s3
	s_max_i32 s2, s13, 0
	s_lshl_b64 s[10:11], s[22:23], 20
	s_lshl_b64 s[2:3], s[2:3], 14
	v_mov_b32_e32 v75, 0
	v_lshl_add_u64 v[76:77], v[74:75], 1, s[6:7]
	s_movk_i32 s6, 0x2000
	s_add_u32 s23, s4, s10
	v_lshrrev_b32_e32 v71, 4, v0
	v_add_co_u32_e32 v10, vcc, s6, v76
	s_addc_u32 s28, s5, s11
	v_add_u32_e32 v84, -3, v71
	v_addc_co_u32_e32 v11, vcc, 0, v77, vcc
	s_add_u32 s2, s23, s2
	v_max_i32_e32 v86, 0, v84
	global_load_dwordx4 v[6:9], v[10:11], off offset:-4096
	global_load_dwordx4 v[2:5], v[10:11], off
	s_addc_u32 s3, s28, s3
	v_lshlrev_b32_e32 v10, 8, v86
	v_mov_b32_e32 v11, v75
	v_and_b32_e32 v97, 0x78, v74
	v_lshl_add_u64 v[10:11], s[2:3], 0, v[10:11]
	v_lshlrev_b32_e32 v74, 1, v97
	v_lshl_add_u64 v[106:107], v[10:11], 0, v[74:75]
	v_or_b32_e32 v10, 0x100, v0
	v_lshrrev_b32_e32 v98, 4, v10
	v_add_u32_e32 v85, -3, v98
	v_and_b32_e32 v82, 0x78, v1
	v_or_b32_e32 v1, 0x200, v0
	v_lshlrev_b32_e32 v10, 8, v85
	v_mov_b32_e32 v11, v75
	v_lshrrev_b32_e32 v99, 4, v1
	s_movk_i32 s6, 0x4000
	v_lshl_add_u64 v[10:11], s[2:3], 0, v[10:11]
	v_lshlrev_b32_e32 v12, 1, v82
	v_mov_b32_e32 v13, v75
	v_add_u32_e32 v89, -3, v99
	v_or_b32_e32 v1, 0x300, v0
	v_add_co_u32_e32 v80, vcc, s6, v76
	v_lshl_add_u64 v[108:109], v[10:11], 0, v[12:13]
	v_lshlrev_b32_e32 v10, 8, v89
	v_mov_b32_e32 v11, v75
	v_lshrrev_b32_e32 v96, 4, v1
	v_addc_co_u32_e32 v81, vcc, 0, v77, vcc
	s_movk_i32 s6, 0x6000
	v_lshl_add_u64 v[10:11], s[2:3], 0, v[10:11]
	v_add_u32_e32 v90, -3, v96
	v_add_co_u32_e32 v94, vcc, s6, v76
	v_lshl_add_u64 v[110:111], v[10:11], 0, v[12:13]
	v_lshlrev_b32_e32 v10, 8, v90
	v_mov_b32_e32 v11, v75
	v_or_b32_e32 v93, 0x400, v0
	v_addc_co_u32_e32 v95, vcc, 0, v77, vcc
	s_mov_b32 s6, 0x8000
	v_lshl_add_u64 v[10:11], s[2:3], 0, v[10:11]
	v_min_u32_e32 v1, 0x45f, v93
	v_add_co_u32_e32 v100, vcc, s6, v76
	v_lshl_add_u64 v[112:113], v[10:11], 0, v[12:13]
	v_lshrrev_b32_e32 v10, 4, v1
	v_addc_co_u32_e32 v101, vcc, 0, v77, vcc
	s_mov_b32 s6, 0xa000
	v_add_u32_e32 v91, -3, v10
	v_add_co_u32_e32 v102, vcc, s6, v76
	v_min_u32_e32 v92, 63, v91
	v_lshlrev_b32_e32 v1, 3, v1
	v_addc_co_u32_e32 v103, vcc, 0, v77, vcc
	s_mov_b32 s6, 0xb000
	v_lshlrev_b32_e32 v10, 8, v92
	v_mov_b32_e32 v11, v75
	v_and_b32_e32 v1, 0x78, v1
	v_add_co_u32_e32 v104, vcc, s6, v76
	v_lshl_add_u64 v[10:11], s[2:3], 0, v[10:11]
	v_lshlrev_b32_e32 v78, 1, v1
	v_mov_b32_e32 v79, v75
	v_addc_co_u32_e32 v105, vcc, 0, v77, vcc
	v_lshl_add_u64 v[114:115], v[10:11], 0, v[78:79]
	global_load_dwordx4 v[58:61], v[80:81], off offset:-4096
	global_load_dwordx4 v[54:57], v[80:81], off
	global_load_dwordx4 v[50:53], v[94:95], off offset:-4096
	global_load_dwordx4 v[46:49], v[94:95], off
	global_load_dwordx4 v[38:41], v[100:101], off offset:-4096
	global_load_dwordx4 v[42:45], v[100:101], off
	global_load_dwordx4 v[30:33], v[102:103], off offset:-4096
	global_load_dwordx4 v[26:29], v[102:103], off
	global_load_dwordx4 v[66:69], v[106:107], off
	global_load_dwordx4 v[22:25], v[108:109], off
	global_load_dwordx4 v[18:21], v[110:111], off
	global_load_dwordx4 v[14:17], v[112:113], off
	global_load_dwordx4 v[10:13], v[114:115], off
	global_load_dwordx4 v[34:37], v[104:105], off
	global_load_dwordx4 v[62:65], v[76:77], off
	v_and_b32_e32 v95, 31, v0
	v_lshrrev_b32_e32 v1, 2, v0
	v_and_or_b32 v70, v1, 32, v95
	v_add_u32_e32 v79, s27, v72
	v_add_u32_e32 v94, v72, v70
	v_cmp_gt_u32_e64 s[6:7], 64, v79
	v_cmp_gt_u32_e64 s[2:3], 64, v94
	s_movk_i32 s10, 0x100
	s_and_b64 s[14:15], s[6:7], s[2:3]
	v_lshlrev_b32_e32 v1, 6, v79
	v_mov_b64_e32 v[72:73], 0
	v_add_u32_e32 v1, s12, v70
	v_cmp_gt_u32_e32 vcc, 64, v1
	v_add_u32_e32 v80, s26, v70
	s_add_i32 s29, s27, s12
	s_cmp_lt_u32 s29, 64
	s_cselect_b64 s[24:25], -1, 0
	v_max_i32_e32 v116, 0, v79
	v_max_i32_e32 v117, 0, v94
	v_min_u32_e32 v118, 63, v1
	s_min_u32 s10, s29, 63
	s_lshl_b32 s10, s10, 6
	s_lshl_b32 s11, s27, 6
	v_lshl_or_b32 v116, v116, 6, v83
	v_or_b32_e32 v119, s11, v83
	v_or_b32_e32 v120, s10, v83
	v_add_lshl_u32 v121, v116, v117, 3
	global_load_dwordx2 v[122:123], v121, s[8:9]
	v_add_lshl_u32 v121, v116, v70, 3
	global_load_dwordx2 v[124:125], v121, s[8:9]
	v_add_lshl_u32 v121, v116, v118, 3
	global_load_dwordx2 v[126:127], v121, s[8:9]
	v_add_lshl_u32 v121, v119, v117, 3
	global_load_dwordx2 v[128:129], v121, s[8:9]
	v_add_lshl_u32 v121, v119, v70, 3
	global_load_dwordx2 v[130:131], v121, s[8:9]
	v_add_lshl_u32 v121, v119, v118, 3
	global_load_dwordx2 v[132:133], v121, s[8:9]
	v_add_lshl_u32 v121, v120, v117, 3
	global_load_dwordx2 v[134:135], v121, s[8:9]
	v_add_lshl_u32 v121, v120, v70, 3
	global_load_dwordx2 v[136:137], v121, s[8:9]
	v_add_lshl_u32 v121, v120, v118, 3
	global_load_dwordx2 v[138:139], v121, s[8:9]
	v_lshlrev_b32_e32 v75, 7, v86
	v_lshlrev_b32_e32 v88, 7, v85
	v_lshlrev_b32_e32 v87, 7, v89
	v_lshlrev_b32_e32 v86, 7, v90
	v_lshlrev_b32_e32 v79, 7, v92
	s_and_b64 s[14:15], s[6:7], s[2:3]
	s_and_b64 s[4:5], s[6:7], vcc
	s_and_b64 s[16:17], s[24:25], s[2:3]
	s_and_b64 s[18:19], s[24:25], vcc
	s_waitcnt vmcnt(0)
	v_cndmask_b32_e64 v122, 0, v122, s[14:15]
	v_cndmask_b32_e64 v123, 0, v123, s[14:15]
	v_add_f64 v[72:73], v[122:123], 0
	v_cndmask_b32_e64 v124, 0, v124, s[6:7]
	v_cndmask_b32_e64 v125, 0, v125, s[6:7]
	v_add_f64 v[72:73], v[72:73], v[124:125]
	v_cndmask_b32_e64 v126, 0, v126, s[4:5]
	v_cndmask_b32_e64 v127, 0, v127, s[4:5]
	v_add_f64 v[72:73], v[72:73], v[126:127]
	v_cndmask_b32_e64 v128, 0, v128, s[2:3]
	v_cndmask_b32_e64 v129, 0, v129, s[2:3]
	v_add_f64 v[72:73], v[72:73], v[128:129]
	v_add_f64 v[72:73], v[72:73], v[130:131]
	v_cndmask_b32_e64 v132, 0, v132, vcc
	v_cndmask_b32_e64 v133, 0, v133, vcc
	v_add_f64 v[72:73], v[72:73], v[132:133]
	v_cndmask_b32_e64 v134, 0, v134, s[16:17]
	v_cndmask_b32_e64 v135, 0, v135, s[16:17]
	v_add_f64 v[72:73], v[72:73], v[134:135]
	v_cndmask_b32_e64 v136, 0, v136, s[24:25]
	v_cndmask_b32_e64 v137, 0, v137, s[24:25]
	v_add_f64 v[72:73], v[72:73], v[136:137]
	v_cndmask_b32_e64 v138, 0, v138, s[18:19]
	v_cndmask_b32_e64 v139, 0, v139, s[18:19]
	v_add_f64 v[72:73], v[72:73], v[138:139]
	s_cmp_gt_i32 s13, -1
	s_cselect_b64 s[12:13], -1, 0
	v_cmp_gt_u32_e64 s[10:11], 64, v84
	v_cmp_gt_u32_e64 s[8:9], 64, v85
	v_cmp_gt_u32_e64 s[6:7], 64, v89
	v_cmp_gt_u32_e64 s[4:5], 64, v90
	v_cmp_gt_u32_e64 s[2:3], 64, v91
	s_and_b64 vcc, exec, s[12:13]
	v_lshrrev_b32_e32 v100, 4, v93
	s_cbranch_vccz .LBB1_29
	s_waitcnt vmcnt(6)
	v_cndmask_b32_e64 v102, 0, v66, s[10:11]
	v_mov_b32_e32 v66, 0x100
	v_lshl_add_u32 v66, v97, 1, v66
	s_movk_i32 s14, 0x110
	v_cndmask_b32_e64 v103, 0, v67, s[10:11]
	v_mad_u32_u24 v67, v71, s14, v66
	s_waitcnt vmcnt(0)
	ds_write_b128 v67, v[62:65] offset:19040
	v_mad_u32_u24 v62, v98, s14, v66
	ds_write_b128 v62, v[6:9] offset:19040
	v_mad_u32_u24 v6, v99, s14, v66
	ds_write_b128 v6, v[2:5] offset:19040
	v_mad_u32_u24 v2, v96, s14, v66
	ds_write_b128 v2, v[58:61] offset:19040
	v_mad_u32_u24 v2, v100, s14, v66
	ds_write_b128 v2, v[54:57] offset:19040
	v_or_b32_e32 v2, 0x500, v0
	v_lshrrev_b32_e32 v2, 4, v2
	v_mad_u32_u24 v2, v2, s14, v66
	ds_write_b128 v2, v[50:53] offset:19040
	v_or_b32_e32 v2, 0x600, v0
	v_lshrrev_b32_e32 v2, 4, v2
	v_mad_u32_u24 v2, v2, s14, v66
	ds_write_b128 v2, v[46:49] offset:19040
	v_or_b32_e32 v2, 0x700, v0
	v_lshrrev_b32_e32 v2, 4, v2
	v_mad_u32_u24 v2, v2, s14, v66
	ds_write_b128 v2, v[38:41] offset:19040
	ds_write_b128 v67, v[42:45] offset:53856
	v_or_b32_e32 v2, 0x900, v0
	v_lshrrev_b32_e32 v2, 4, v2
	v_mad_u32_u24 v2, v2, s14, v66
	ds_write_b128 v2, v[30:33] offset:19040
	v_or_b32_e32 v2, 0xa00, v0
	v_lshrrev_b32_e32 v2, 4, v2
	v_mad_u32_u24 v2, v2, s14, v66
	ds_write_b128 v2, v[26:29] offset:19040
	v_or_b32_e32 v2, 0xb00, v0
	v_lshrrev_b32_e32 v2, 4, v2
	v_mad_u32_u24 v2, v2, s14, v66
	s_movk_i32 s14, 0x360
	v_cmp_gt_u32_e32 vcc, s14, v0
	v_cndmask_b32_e64 v105, 0, v69, s[10:11]
	v_cndmask_b32_e64 v104, 0, v68, s[10:11]
	ds_write_b128 v2, v[34:37] offset:19040
	ds_write_b128 v67, v[102:105]
	s_and_saveexec_b64 s[14:15], vcc
	s_cbranch_execz .LBB1_22
	v_mul_u32_u24_e32 v6, 0x110, v98
	v_cndmask_b32_e64 v5, 0, v25, s[8:9]
	v_cndmask_b32_e64 v4, 0, v24, s[8:9]
	v_cndmask_b32_e64 v3, 0, v23, s[8:9]
	v_cndmask_b32_e64 v2, 0, v22, s[8:9]
	v_add_u32_e32 v6, v66, v6
	ds_write_b128 v6, v[2:5]

.LBB1_48:
	s_mov_b32 s2, 0
	s_brev_b32 s3, 8
	s_waitcnt vmcnt(0)
	v_mov_b32_e32 v0, 0x100
	v_cmp_gt_f64_e32 vcc, s[2:3], v[72:73]
	s_mov_b32 s2, 0x812dea11
	s_mov_b32 s3, 0x3d719799
	v_cndmask_b32_e32 v0, 0, v0, vcc
	v_ldexp_f64 v[0:1], v[72:73], v0
	v_rsq_f64_e32 v[2:3], v[0:1]
	s_lshl_b32 s4, s22, 6
	v_lshlrev_b32_e32 v16, 4, v92
	v_lshl_add_u32 v31, v17, 2, v16
	v_mul_f64 v[4:5], v[0:1], v[2:3]
	v_mul_f64 v[2:3], v[2:3], 0.5
	v_fma_f64 v[6:7], -v[2:3], v[4:5], 0.5
	v_fmac_f64_e32 v[4:5], v[4:5], v[6:7]
	v_fma_f64 v[8:9], -v[4:5], v[4:5], v[0:1]
	v_fmac_f64_e32 v[2:3], v[2:3], v[6:7]
	v_fmac_f64_e32 v[4:5], v[8:9], v[2:3]
	v_fma_f64 v[6:7], -v[4:5], v[4:5], v[0:1]
	v_fmac_f64_e32 v[4:5], v[6:7], v[2:3]
	v_mov_b32_e32 v2, 0xffffff80
	v_cndmask_b32_e32 v2, 0, v2, vcc
	v_ldexp_f64 v[2:3], v[4:5], v2
	v_mov_b32_e32 v4, 0x260
	v_cmp_class_f64_e32 vcc, v[0:1], v4
	s_nop 1
	v_cndmask_b32_e32 v1, v3, v1, vcc
	v_cndmask_b32_e32 v0, v2, v0, vcc
	v_max_f64 v[18:19], v[0:1], s[2:3]
	v_div_scale_f64 v[20:21], s[2:3], v[18:19], v[18:19], 1.0
	v_rcp_f64_e32 v[22:23], v[20:21]
	s_lshl_b32 s2, s26, 7
	s_add_i32 s2, s2, s4
	s_mov_b32 s3, 0
	v_fma_f64 v[24:25], -v[20:21], v[22:23], 1.0
	v_fmac_f64_e32 v[22:23], v[22:23], v[24:25]
	v_fma_f64 v[24:25], -v[20:21], v[22:23], 1.0
	v_fmac_f64_e32 v[22:23], v[22:23], v[24:25]
	v_div_scale_f64 v[24:25], vcc, 1.0, v[18:19], 1.0
	v_mul_f64 v[26:27], v[24:25], v[22:23]
	v_fma_f64 v[20:21], -v[20:21], v[26:27], v[24:25]
	v_or_b32_e32 v24, s2, v17
	s_nop 0
	v_div_fmas_f64 v[20:21], v[20:21], v[22:23], v[26:27]
	v_div_fixup_f64 v[18:19], v[20:21], v[18:19], 1.0
	v_mov_b32_e32 v25, 0
	v_cvt_f32_f64_e32 v30, v[18:19]
	v_lshlrev_b64 v[18:19], 14, v[24:25]
	v_lshl_add_u64 v[18:19], s[0:1], 0, v[18:19]
	s_lshl_b32 s2, s27, 8
	v_lshl_add_u64 v[20:21], v[18:19], 0, s[2:3]
	ds_read_b128 v[16:19], v31
	v_accvgpr_read_b32 v0, a0
	v_mov_b32_e32 v71, v25
	v_lshl_add_u64 v[26:27], v[70:71], 2, v[20:21]
	v_mul_f32_e32 v0, v0, v30
	v_lshlrev_b32_e32 v24, 16, v92
	v_accvgpr_read_b32 v1, a1
	ds_read_b128 v[20:23], v31 offset:32
	s_waitcnt lgkmcnt(1)
	v_mul_f32_e32 v0, v0, v16
	v_lshl_add_u64 v[28:29], v[26:27], 0, v[24:25]
	global_store_dword v[28:29], v0, off
	v_mul_f32_e32 v0, v1, v30
	v_mul_f32_e32 v16, v0, v17
	v_or_b32_e32 v0, 0x4000, v24
	v_mov_b32_e32 v1, v25
	v_accvgpr_read_b32 v2, a2
	v_lshl_add_u64 v[0:1], v[26:27], 0, v[0:1]
	global_store_dword v[0:1], v16, off
	v_mul_f32_e32 v0, v2, v30
	v_mul_f32_e32 v2, v0, v18
	v_or_b32_e32 v0, 0x8000, v24
	v_mov_b32_e32 v1, v25
	v_accvgpr_read_b32 v3, a3
	v_lshl_add_u64 v[0:1], v[26:27], 0, v[0:1]
	global_store_dword v[0:1], v2, off
	v_mul_f32_e32 v0, v3, v30
	v_mul_f32_e32 v2, v0, v19
	v_or_b32_e32 v0, 0xc000, v24
	v_mov_b32_e32 v1, v25
	v_accvgpr_read_b32 v4, a4
	v_lshl_add_u64 v[0:1], v[26:27], 0, v[0:1]
	global_store_dword v[0:1], v2, off
	v_mul_f32_e32 v0, v4, v30
	s_waitcnt lgkmcnt(0)
	v_mul_f32_e32 v2, v0, v20
	v_or_b32_e32 v0, 0x20000, v24
	v_mov_b32_e32 v1, v25
	v_accvgpr_read_b32 v5, a5
	v_lshl_add_u64 v[0:1], v[26:27], 0, v[0:1]
	global_store_dword v[0:1], v2, off
	v_mul_f32_e32 v0, v5, v30
	v_mul_f32_e32 v2, v0, v21
	v_or_b32_e32 v0, 0x24000, v24
	v_mov_b32_e32 v1, v25
	v_accvgpr_read_b32 v6, a6
	v_lshl_add_u64 v[0:1], v[26:27], 0, v[0:1]
	global_store_dword v[0:1], v2, off
	v_mul_f32_e32 v0, v6, v30
	v_mul_f32_e32 v2, v0, v22
	v_or_b32_e32 v0, 0x28000, v24
	v_mov_b32_e32 v1, v25
	v_accvgpr_read_b32 v7, a7
	v_lshl_add_u64 v[0:1], v[26:27], 0, v[0:1]
	global_store_dword v[0:1], v2, off
	v_mul_f32_e32 v0, v7, v30
	v_mul_f32_e32 v6, v0, v23
	ds_read_b128 v[0:3], v31 offset:64
	v_accvgpr_read_b32 v8, a8
	v_or_b32_e32 v4, 0x2c000, v24
	v_mov_b32_e32 v5, v25
	v_lshl_add_u64 v[4:5], v[26:27], 0, v[4:5]
	v_mul_f32_e32 v8, v8, v30
	v_or_b32_e32 v16, 0x40000, v24
	v_mov_b32_e32 v17, v25
	v_accvgpr_read_b32 v9, a9
	global_store_dword v[4:5], v6, off
	ds_read_b128 v[4:7], v31 offset:96
	s_waitcnt lgkmcnt(1)
	v_mul_f32_e32 v0, v8, v0
	v_lshl_add_u64 v[16:17], v[26:27], 0, v[16:17]
	global_store_dword v[16:17], v0, off
	v_mul_f32_e32 v0, v9, v30
	v_mul_f32_e32 v8, v0, v1
	v_or_b32_e32 v0, 0x44000, v24
	v_mov_b32_e32 v1, v25
	v_accvgpr_read_b32 v10, a10
	v_lshl_add_u64 v[0:1], v[26:27], 0, v[0:1]
	global_store_dword v[0:1], v8, off
	v_mul_f32_e32 v0, v10, v30
	v_mul_f32_e32 v2, v0, v2
	v_or_b32_e32 v0, 0x48000, v24
	v_mov_b32_e32 v1, v25
	v_accvgpr_read_b32 v11, a11
	v_lshl_add_u64 v[0:1], v[26:27], 0, v[0:1]
	global_store_dword v[0:1], v2, off
	v_mul_f32_e32 v0, v11, v30
	v_mul_f32_e32 v2, v0, v3
	v_or_b32_e32 v0, 0x4c000, v24
	v_mov_b32_e32 v1, v25
	v_accvgpr_read_b32 v12, a12
	v_lshl_add_u64 v[0:1], v[26:27], 0, v[0:1]
	global_store_dword v[0:1], v2, off
	v_mul_f32_e32 v0, v12, v30
	s_waitcnt lgkmcnt(0)
	v_mul_f32_e32 v2, v0, v4
	v_or_b32_e32 v0, 0x60000, v24
	v_mov_b32_e32 v1, v25
	v_accvgpr_read_b32 v13, a13
	v_lshl_add_u64 v[0:1], v[26:27], 0, v[0:1]
	global_store_dword v[0:1], v2, off
	v_mul_f32_e32 v0, v13, v30
	v_mul_f32_e32 v2, v0, v5
	v_or_b32_e32 v0, 0x64000, v24
	v_mov_b32_e32 v1, v25
	v_accvgpr_read_b32 v14, a14
	v_lshl_add_u64 v[0:1], v[26:27], 0, v[0:1]
	global_store_dword v[0:1], v2, off
	v_mul_f32_e32 v0, v14, v30
	v_mul_f32_e32 v2, v0, v6
	v_or_b32_e32 v0, 0x68000, v24
	v_mov_b32_e32 v1, v25
	v_accvgpr_read_b32 v15, a15
	v_lshl_add_u64 v[0:1], v[26:27], 0, v[0:1]
	global_store_dword v[0:1], v2, off
	v_mul_f32_e32 v0, v15, v30
	v_or_b32_e32 v24, 0x6c000, v24
	v_mul_f32_e32 v2, v0, v7
	v_lshl_add_u64 v[0:1], v[26:27], 0, v[24:25]
	global_store_dword v[0:1], v2, off
	s_endpgm
.LBB1_52:
	v_mov_b32_e32 v81, v83
	v_lshl_add_u64 v[22:23], s[24:25], 0, v[80:81]
	v_lshl_add_u64 v[22:23], v[22:23], 0, v[82:83]
	global_load_dwordx4 v[22:25], v[22:23], off
	s_waitcnt vmcnt(0)
	v_cndmask_b32_e64 v25, 0, v25, s[8:9]
	v_cndmask_b32_e64 v24, 0, v24, s[8:9]
	v_cndmask_b32_e64 v23, 0, v23, s[8:9]
	v_cndmask_b32_e64 v22, 0, v22, s[8:9]
	ds_write_b128 v18, v[22:25]
	s_or_b64 exec, exec, s[10:11]
	s_and_saveexec_b64 s[8:9], s[12:13]
	s_cbranch_execz .LBB1_42

	.amdhsa_kernel _Z9k_coarse2PKtS0_PKdS2_Pf
		.amdhsa_group_segment_fixed_size 256
		.amdhsa_private_segment_fixed_size 0
		.amdhsa_kernarg_size 40
		.amdhsa_user_sgpr_count 2
		.amdhsa_user_sgpr_dispatch_ptr 0
		.amdhsa_user_sgpr_queue_ptr 0
		.amdhsa_user_sgpr_kernarg_segment_ptr 1
		.amdhsa_user_sgpr_dispatch_id 0
		.amdhsa_user_sgpr_kernarg_preload_length 0
		.amdhsa_user_sgpr_kernarg_preload_offset 0
		.amdhsa_user_sgpr_private_segment_size 0
		.amdhsa_uses_dynamic_stack 0
		.amdhsa_enable_private_segment 0
		.amdhsa_system_sgpr_workgroup_id_x 1
		.amdhsa_system_sgpr_workgroup_id_y 0
		.amdhsa_system_sgpr_workgroup_id_z 0
		.amdhsa_system_sgpr_workgroup_info 0
		.amdhsa_system_vgpr_workitem_id 0
		.amdhsa_next_free_vgpr 156
		.amdhsa_next_free_sgpr 31
		.amdhsa_accum_offset 140
		.amdhsa_reserve_vcc 1
		.amdhsa_float_round_mode_32 0
		.amdhsa_float_round_mode_16_64 0
		.amdhsa_float_denorm_mode_32 3
		.amdhsa_float_denorm_mode_16_64 3
		.amdhsa_dx10_clamp 1
		.amdhsa_ieee_mode 1
		.amdhsa_fp16_overflow 0
		.amdhsa_tg_split 0
		.amdhsa_exception_fp_ieee_invalid_op 0
		.amdhsa_exception_fp_denorm_src 0
		.amdhsa_exception_fp_ieee_div_zero 0
		.amdhsa_exception_fp_ieee_overflow 0
		.amdhsa_exception_fp_ieee_underflow 0
		.amdhsa_exception_fp_ieee_inexact 0
		.amdhsa_exception_int_div_zero 0
	.end_amdhsa_kernel

_Z7k_fine3PKfS0_PKtS2_PKdS4_S0_PiPfS5_S0_S0_PtS7_:
	s_load_dwordx2 s[4:5], s[0:1], 0x30
	s_load_dwordx8 s[68:75], s[0:1], 0x0
	s_load_dwordx2 s[88:89], s[0:1], 0x48
	s_load_dwordx4 s[80:83], s[0:1], 0x20
	s_load_dwordx8 s[60:67], s[0:1], 0x50
	s_lshl_b32 s3, s2, 5
	s_and_b32 s3, s3, 0xe0
	s_lshr_b32 s76, s2, 3
	s_add_i32 s3, s3, s76
	s_lshr_b32 s84, s3, 1
	s_mov_b32 s85, 0
	s_lshl_b64 s[6:7], s[84:85], 14
	s_waitcnt lgkmcnt(0)
	s_add_u32 s4, s4, s6
	s_addc_u32 s5, s5, s7
	v_lshlrev_b32_e32 v2, 2, v0
	v_mov_b32_e32 v3, 0
	v_lshl_add_u64 v[4:5], s[4:5], 0, v[2:3]
	s_mov_b32 s6, 0x200000
	v_add_co_u32_e32 v6, vcc, s6, v4
	s_mov_b32 s7, 0x400000
	s_nop 0
	v_addc_co_u32_e32 v7, vcc, 0, v5, vcc
	v_or_b32_e32 v117, 0x400, v0
	v_add_co_u32_e32 v8, vcc, s7, v4
	v_lshlrev_b32_e32 v10, 2, v117
	v_mov_b32_e32 v11, v3
	v_addc_co_u32_e32 v9, vcc, 0, v5, vcc
	v_lshl_add_u64 v[12:13], s[4:5], 0, v[10:11]
	v_add_co_u32_e32 v14, vcc, s6, v12
	s_movk_i32 s8, 0x1000
	s_nop 0
	v_addc_co_u32_e32 v15, vcc, 0, v13, vcc
	v_add_co_u32_e32 v12, vcc, s7, v12
	v_or_b32_e32 v118, 0x800, v0
	s_nop 0
	v_addc_co_u32_e32 v13, vcc, 0, v13, vcc
	v_add_co_u32_e32 v16, vcc, s8, v4
	s_mov_b32 s8, 0x201000
	s_nop 0
	v_addc_co_u32_e32 v17, vcc, 0, v5, vcc
	v_add_co_u32_e32 v18, vcc, s8, v4
	s_mov_b32 s8, 0x401000
	s_nop 0
	v_addc_co_u32_e32 v19, vcc, 0, v5, vcc
	global_load_dword v24, v[6:7], off nt
	global_load_dword v25, v[8:9], off nt
	global_load_dword v26, v[8:9], off offset:2048 nt
	global_load_dword v27, v[14:15], off nt
	global_load_dword v28, v[12:13], off nt
	global_load_dword v29, v[16:17], off offset:2048 nt
	global_load_dword v30, v[18:19], off offset:2048 nt
	global_load_dword v31, v[6:7], off offset:2048 nt
	v_add_co_u32_e32 v6, vcc, s8, v4
	v_lshlrev_b32_e32 v8, 2, v118
	v_mov_b32_e32 v9, v3
	v_addc_co_u32_e32 v7, vcc, 0, v5, vcc
	v_lshl_add_u64 v[12:13], s[4:5], 0, v[8:9]
	global_load_dword v32, v2, s[4:5] nt
	global_load_dword v33, v2, s[4:5] offset:2048 nt
	global_load_dword v34, v10, s[4:5] nt
	global_load_dword v35, v8, s[4:5] nt
	v_add_co_u32_e32 v8, vcc, s6, v12
	s_movk_i32 s8, 0x2000
	s_nop 0
	v_addc_co_u32_e32 v9, vcc, 0, v13, vcc
	v_add_co_u32_e32 v10, vcc, s7, v12
	v_or_b32_e32 v1, 0xc00, v0
	s_nop 0
	v_addc_co_u32_e32 v11, vcc, 0, v13, vcc
	v_add_co_u32_e32 v12, vcc, s8, v4
	s_mov_b32 s8, 0x202000
	s_nop 0
	v_addc_co_u32_e32 v13, vcc, 0, v5, vcc
	v_add_co_u32_e32 v14, vcc, s8, v4
	s_mov_b32 s8, 0x402000
	s_nop 0
	v_addc_co_u32_e32 v15, vcc, 0, v5, vcc
	v_add_co_u32_e32 v16, vcc, s8, v4
	v_lshlrev_b32_e32 v18, 2, v1
	v_mov_b32_e32 v19, v3
	v_addc_co_u32_e32 v17, vcc, 0, v5, vcc
	v_lshl_add_u64 v[20:21], s[4:5], 0, v[18:19]
	v_add_co_u32_e32 v22, vcc, s6, v20
	s_movk_i32 s6, 0x3000
	s_nop 0
	v_addc_co_u32_e32 v23, vcc, 0, v21, vcc
	v_add_co_u32_e32 v20, vcc, s7, v20
	v_and_b32_e32 v124, 63, v0
	s_nop 0
	v_addc_co_u32_e32 v21, vcc, 0, v21, vcc
	global_load_dword v3, v[6:7], off offset:2048 nt
	global_load_dword v19, v[8:9], off nt
	global_load_dword v36, v[10:11], off nt
	global_load_dword v37, v[12:13], off offset:2048 nt
	global_load_dword v38, v[14:15], off offset:2048 nt
	global_load_dword v39, v[16:17], off offset:2048 nt
	global_load_dword v40, v[22:23], off nt
	global_load_dword v41, v[20:21], off nt
	v_add_co_u32_e32 v6, vcc, s6, v4
	s_mov_b32 s6, 0x203000
	s_nop 0
	v_addc_co_u32_e32 v7, vcc, 0, v5, vcc
	v_add_co_u32_e32 v8, vcc, s6, v4
	s_mov_b32 s6, 0x403000
	s_nop 0
	v_addc_co_u32_e32 v9, vcc, 0, v5, vcc
	v_add_co_u32_e32 v4, vcc, s6, v4
	v_lshrrev_b32_e32 v116, 6, v0
	s_nop 0
	v_addc_co_u32_e32 v5, vcc, 0, v5, vcc
	global_load_dword v13, v18, s[4:5] nt
	global_load_dword v14, v[6:7], off offset:2048 nt
	global_load_dword v15, v[8:9], off offset:2048 nt
	global_load_dword v16, v[4:5], off offset:2048 nt
	s_and_b32 s90, s84, 56
	s_lshl_b32 s91, s84, 3
	s_and_b32 s91, s91, 56
	s_or_b32 s90, s90, 4
	s_or_b32 s91, s91, 4
	s_lshr_b32 s92, s3, 7
	s_lshl_b32 s92, s92, 12
	v_lshrrev_b32_e32 v216, 5, v0
	v_mul_u32_u24_e32 v217, 57, v216
	v_lshrrev_b32_e32 v217, 9, v217
	v_mad_i32_i24 v216, v217, -9, v216
	v_add_u32_e32 v218, 1, v217
	v_mul_u32_u24_e32 v217, 0xab, v216
	v_lshrrev_b32_e32 v217, 9, v217
	v_mad_i32_i24 v216, v217, -3, v216
	v_add_u32_e32 v217, -1, v217
	v_add_u32_e32 v216, -1, v216
	v_mad_i32_i24 v217, v217, v218, s90
	v_mad_i32_i24 v216, v216, v218, s91
	v_lshl_add_u32 v217, v217, 6, v216
	v_add_u32_e32 v217, s92, v217
	v_and_b32_e32 v216, 31, v0
	v_lshlrev_b32_e32 v217, 9, v217
	v_lshl_add_u32 v217, v216, 4, v217
	global_load_dwordx4 v[220:223], v217, s[68:69]
	v_add_u32_e32 v219, 0x200, v0
	v_min_u32_e32 v219, 0x35f, v219
	v_lshrrev_b32_e32 v216, 5, v219
	v_mul_u32_u24_e32 v217, 57, v216
	v_lshrrev_b32_e32 v217, 9, v217
	v_mad_i32_i24 v216, v217, -9, v216
	v_add_u32_e32 v218, 1, v217
	v_mul_u32_u24_e32 v217, 0xab, v216
	v_lshrrev_b32_e32 v217, 9, v217
	v_mad_i32_i24 v216, v217, -3, v216
	v_add_u32_e32 v217, -1, v217
	v_add_u32_e32 v216, -1, v216
	v_mad_i32_i24 v217, v217, v218, s90
	v_mad_i32_i24 v216, v216, v218, s91
	v_lshl_add_u32 v217, v217, 6, v216
	v_add_u32_e32 v217, s92, v217
	v_and_b32_e32 v216, 31, v219
	v_lshlrev_b32_e32 v217, 9, v217
	v_lshl_add_u32 v217, v216, 4, v217
	global_load_dwordx4 v[224:227], v217, s[68:69]
	s_mov_b32 s4, 0xff800000
	v_cmp_eq_u32_e64 s[42:43], 0, v124
	s_waitcnt vmcnt(17)
	v_add_f32_e32 v4, v32, v24
	v_add_f32_e32 v12, v4, v25
	s_waitcnt vmcnt(16)
	v_add_f32_e32 v4, v33, v31
	s_waitcnt vmcnt(15)
	v_add_f32_e32 v5, v34, v27
	v_add_f32_e32 v11, v4, v26
	v_add_f32_e32 v10, v5, v28
	v_add_f32_e32 v5, v29, v30
	v_max3_f32 v4, v12, s4, v11
	s_waitcnt vmcnt(13)
	v_add_f32_e32 v9, v5, v3
	v_max3_f32 v3, v4, v10, v9
	s_waitcnt vmcnt(12)
	v_add_f32_e32 v4, v35, v19
	s_waitcnt vmcnt(11)
	v_add_f32_e32 v8, v4, v36
	s_waitcnt vmcnt(9)
	v_add_f32_e32 v4, v37, v38
	v_mbcnt_lo_u32_b32 v5, -1, 0
	s_waitcnt vmcnt(8)
	v_add_f32_e32 v7, v4, v39
	v_mbcnt_hi_u32_b32 v5, -1, v5
	v_max3_f32 v4, v3, v8, v7
	s_waitcnt vmcnt(5)
	v_add_f32_e32 v3, v13, v40
	v_and_b32_e32 v13, 64, v5
	v_add_f32_e32 v6, v3, v41
	s_waitcnt vmcnt(3)
	v_add_f32_e32 v3, v14, v15
	v_add_u32_e32 v13, 64, v13
	v_xor_b32_e32 v14, 1, v5
	v_cmp_lt_i32_e32 vcc, v14, v13
	s_waitcnt vmcnt(2)
	v_add_f32_e32 v3, v3, v16
	v_max3_f32 v4, v4, v6, v3
	v_cndmask_b32_e32 v14, v5, v14, vcc
	v_lshlrev_b32_e32 v115, 2, v14
	s_nop 1
	v_mov_b32_dpp v14, v4 quad_perm:[1,0,3,2] row_mask:0xf bank_mask:0xf
	s_waitcnt lgkmcnt(0)
	v_max_f32_e32 v14, v14, v14
	v_max_f32_e32 v4, v4, v14
	v_xor_b32_e32 v14, 2, v5
	v_cmp_lt_i32_e32 vcc, v14, v13
	s_nop 1
	v_cndmask_b32_e32 v14, v5, v14, vcc
	v_lshlrev_b32_e32 v114, 2, v14
	s_nop 1
	v_mov_b32_dpp v14, v4 quad_perm:[2,3,0,1] row_mask:0xf bank_mask:0xf
	s_waitcnt lgkmcnt(0)
	v_max_f32_e32 v14, v14, v14
	v_max_f32_e32 v4, v4, v14
	v_xor_b32_e32 v14, 4, v5
	v_cmp_lt_i32_e32 vcc, v14, v13
	s_nop 1
	v_cndmask_b32_e32 v14, v5, v14, vcc
	v_lshlrev_b32_e32 v113, 2, v14
	s_nop 1
	v_mov_b32_dpp v14, v4 row_half_mirror row_mask:0xf bank_mask:0xf
	s_waitcnt lgkmcnt(0)
	v_max_f32_e32 v14, v14, v14
	v_max_f32_e32 v4, v4, v14
	v_xor_b32_e32 v14, 8, v5
	v_cmp_lt_i32_e32 vcc, v14, v13
	s_nop 1
	v_cndmask_b32_e32 v14, v5, v14, vcc
	v_lshlrev_b32_e32 v112, 2, v14
	s_nop 1
	v_mov_b32_dpp v14, v4 row_mirror row_mask:0xf bank_mask:0xf
	s_waitcnt lgkmcnt(0)
	v_max_f32_e32 v14, v14, v14
	v_max_f32_e32 v4, v4, v14
	v_xor_b32_e32 v14, 16, v5
	v_cmp_lt_i32_e32 vcc, v14, v13
	s_nop 1
	v_cndmask_b32_e32 v14, v5, v14, vcc
	v_lshlrev_b32_e32 v122, 2, v14
	ds_bpermute_b32 v14, v122, v4
	s_waitcnt lgkmcnt(0)
	v_max_f32_e32 v14, v14, v14
	v_max_f32_e32 v4, v4, v14
	v_xor_b32_e32 v14, 32, v5
	v_cmp_lt_i32_e32 vcc, v14, v13
	s_nop 1
	v_cndmask_b32_e32 v5, v5, v14, vcc
	v_lshlrev_b32_e32 v121, 2, v5
	ds_bpermute_b32 v5, v121, v4
	s_and_saveexec_b64 s[4:5], s[42:43]
	s_cbranch_execz .LBB2_2
	s_waitcnt lgkmcnt(0)
	v_max_f32_e32 v5, v5, v5
	v_max_f32_e32 v4, v4, v4
	v_lshl_add_u32 v13, v116, 2, 0
	v_max_f32_e32 v4, v4, v5
	ds_write_b32 v13, v4 offset:65056

.LBB2_51:
	s_or_b64 exec, exec, s[96:97]
	s_waitcnt vmcnt(7)
	v_cvt_f64_f32_e32 v[92:93], v106
	v_cndmask_b32_e64 v93, 0, v93, s[56:57]
	v_cndmask_b32_e64 v92, 0, v92, s[56:57]
	s_waitcnt lgkmcnt(4)
	v_cvt_f64_f32_e32 v[140:141], v50
	v_cvt_f64_f32_e32 v[106:107], v107
	v_fma_f64 v[92:93], v[92:93], v[140:141], 0
	v_cndmask_b32_e64 v107, 0, v107, s[56:57]
	v_cndmask_b32_e64 v106, 0, v106, s[56:57]
	v_cvt_f64_f32_e32 v[50:51], v51
	v_fmac_f64_e32 v[92:93], v[106:107], v[50:51]
	s_waitcnt vmcnt(6)
	v_cvt_f64_f32_e32 v[50:51], v104
	v_cndmask_b32_e64 v51, 0, v51, s[52:53]
	v_cndmask_b32_e64 v50, 0, v50, s[52:53]
	v_cvt_f64_f32_e32 v[106:107], v52
	v_fmac_f64_e32 v[92:93], v[50:51], v[106:107]
	v_cvt_f64_f32_e32 v[50:51], v105
	v_cndmask_b32_e64 v51, 0, v51, s[52:53]
	v_cndmask_b32_e64 v50, 0, v50, s[52:53]
	v_cvt_f64_f32_e32 v[52:53], v53
	v_fmac_f64_e32 v[92:93], v[50:51], v[52:53]
	s_waitcnt vmcnt(5)
	v_cvt_f64_f32_e32 v[50:51], v100
	v_cndmask_b32_e64 v51, 0, v51, s[50:51]
	v_cndmask_b32_e64 v50, 0, v50, s[50:51]
	s_waitcnt lgkmcnt(3)
	v_cvt_f64_f32_e32 v[52:53], v46
	v_fmac_f64_e32 v[92:93], v[50:51], v[52:53]
	v_cvt_f64_f32_e32 v[50:51], v101
	v_cndmask_b32_e64 v51, 0, v51, s[50:51]
	v_cndmask_b32_e64 v50, 0, v50, s[50:51]
	v_cvt_f64_f32_e32 v[46:47], v47
	v_fmac_f64_e32 v[92:93], v[50:51], v[46:47]
	s_waitcnt vmcnt(4)
	v_cvt_f64_f32_e32 v[46:47], v108
	v_cndmask_b32_e64 v47, 0, v47, s[54:55]
	v_cndmask_b32_e64 v46, 0, v46, s[54:55]
	v_cvt_f64_f32_e32 v[50:51], v48
	v_fmac_f64_e32 v[92:93], v[46:47], v[50:51]
	v_cvt_f64_f32_e32 v[46:47], v109
	v_cndmask_b32_e64 v47, 0, v47, s[54:55]
	v_cndmask_b32_e64 v46, 0, v46, s[54:55]
	v_cvt_f64_f32_e32 v[48:49], v49
	v_fmac_f64_e32 v[92:93], v[46:47], v[48:49]
	v_cvt_f64_f32_e32 v[46:47], v90
	v_cndmask_b32_e64 v47, 0, v47, s[40:41]
	v_cndmask_b32_e64 v46, 0, v46, s[40:41]
	s_waitcnt lgkmcnt(2)
	v_cvt_f64_f32_e32 v[48:49], v42
	v_fmac_f64_e32 v[92:93], v[46:47], v[48:49]
	v_cvt_f64_f32_e32 v[48:49], v91
	v_cndmask_b32_e64 v49, 0, v49, s[40:41]
	v_cndmask_b32_e64 v48, 0, v48, s[40:41]
	v_cvt_f64_f32_e32 v[42:43], v43
	v_fmac_f64_e32 v[92:93], v[48:49], v[42:43]
	s_waitcnt vmcnt(3)
	v_cvt_f64_f32_e32 v[42:43], v102
	v_cndmask_b32_e64 v43, 0, v43, s[46:47]
	v_cndmask_b32_e64 v42, 0, v42, s[46:47]
	v_cvt_f64_f32_e32 v[50:51], v44
	v_fmac_f64_e32 v[92:93], v[42:43], v[50:51]
	v_cvt_f64_f32_e32 v[42:43], v103
	v_cndmask_b32_e64 v43, 0, v43, s[46:47]
	v_cndmask_b32_e64 v42, 0, v42, s[46:47]
	v_cvt_f64_f32_e32 v[44:45], v45
	v_fmac_f64_e32 v[92:93], v[42:43], v[44:45]
	s_waitcnt vmcnt(2)
	v_cvt_f64_f32_e32 v[42:43], v98
	v_cndmask_b32_e64 v43, 0, v43, s[48:49]
	v_cndmask_b32_e64 v42, 0, v42, s[48:49]
	s_waitcnt lgkmcnt(1)
	v_cvt_f64_f32_e32 v[44:45], v38
	v_fmac_f64_e32 v[92:93], v[42:43], v[44:45]
	v_cvt_f64_f32_e32 v[42:43], v99
	v_cndmask_b32_e64 v43, 0, v43, s[48:49]
	v_cndmask_b32_e64 v42, 0, v42, s[48:49]
	v_cvt_f64_f32_e32 v[38:39], v39
	v_fmac_f64_e32 v[92:93], v[42:43], v[38:39]
	s_waitcnt vmcnt(1)
	v_cvt_f64_f32_e32 v[38:39], v96
	v_cndmask_b32_e64 v39, 0, v39, s[0:1]
	v_cndmask_b32_e64 v38, 0, v38, s[0:1]
	v_cvt_f64_f32_e32 v[42:43], v40
	v_fmac_f64_e32 v[92:93], v[38:39], v[42:43]
	v_cvt_f64_f32_e32 v[38:39], v97
	v_cndmask_b32_e64 v39, 0, v39, s[0:1]
	v_cndmask_b32_e64 v38, 0, v38, s[0:1]
	v_cvt_f64_f32_e32 v[40:41], v41
	v_fmac_f64_e32 v[92:93], v[38:39], v[40:41]
	s_waitcnt vmcnt(0)
	v_cvt_f64_f32_e32 v[38:39], v94
	v_cndmask_b32_e64 v39, 0, v39, s[44:45]
	v_cndmask_b32_e64 v38, 0, v38, s[44:45]
	s_waitcnt lgkmcnt(0)
	v_cvt_f64_f32_e32 v[40:41], v110
	v_fmac_f64_e32 v[92:93], v[38:39], v[40:41]
	v_cvt_f64_f32_e32 v[38:39], v95
	v_cndmask_b32_e64 v39, 0, v39, s[44:45]
	v_cndmask_b32_e64 v38, 0, v38, s[44:45]
	v_cvt_f64_f32_e32 v[40:41], v111
	v_fmac_f64_e32 v[92:93], v[38:39], v[40:41]
	v_cvt_f64_f32_e32 v[38:39], v84
	v_cndmask_b32_e64 v39, 0, v39, s[38:39]
	v_cndmask_b32_e64 v38, 0, v38, s[38:39]
	v_cvt_f64_f32_e32 v[40:41], v4
	v_fma_f64 v[38:39], v[38:39], v[40:41], 0
	v_cvt_f64_f32_e32 v[40:41], v85
	v_cndmask_b32_e64 v41, 0, v41, s[38:39]
	v_cndmask_b32_e64 v40, 0, v40, s[38:39]
	v_cvt_f64_f32_e32 v[4:5], v5
	v_fmac_f64_e32 v[38:39], v[40:41], v[4:5]
	v_cvt_f64_f32_e32 v[4:5], v80
	v_cndmask_b32_e64 v5, 0, v5, s[34:35]
	v_cndmask_b32_e64 v4, 0, v4, s[34:35]
	v_cvt_f64_f32_e32 v[40:41], v34
	v_fmac_f64_e32 v[38:39], v[4:5], v[40:41]
	v_cvt_f64_f32_e32 v[4:5], v81
	v_cndmask_b32_e64 v5, 0, v5, s[34:35]
	v_cndmask_b32_e64 v4, 0, v4, s[34:35]
	v_cvt_f64_f32_e32 v[34:35], v35
	v_fmac_f64_e32 v[38:39], v[4:5], v[34:35]
	v_cvt_f64_f32_e32 v[4:5], v76
	v_cndmask_b32_e64 v5, 0, v5, s[30:31]
	v_cndmask_b32_e64 v4, 0, v4, s[30:31]
	v_cvt_f64_f32_e32 v[34:35], v36
	v_fmac_f64_e32 v[38:39], v[4:5], v[34:35]
	v_cvt_f64_f32_e32 v[4:5], v77
	v_cndmask_b32_e64 v5, 0, v5, s[30:31]
	v_cndmask_b32_e64 v4, 0, v4, s[30:31]
	v_cvt_f64_f32_e32 v[34:35], v37
	v_fmac_f64_e32 v[38:39], v[4:5], v[34:35]
	v_cvt_f64_f32_e32 v[4:5], v88
	v_cndmask_b32_e64 v5, 0, v5, s[36:37]
	v_cndmask_b32_e64 v4, 0, v4, s[36:37]
	v_cvt_f64_f32_e32 v[34:35], v30
	v_fmac_f64_e32 v[38:39], v[4:5], v[34:35]
	v_cvt_f64_f32_e32 v[4:5], v89
	v_cndmask_b32_e64 v5, 0, v5, s[36:37]
	v_cndmask_b32_e64 v4, 0, v4, s[36:37]
	v_cvt_f64_f32_e32 v[30:31], v31
	v_fmac_f64_e32 v[38:39], v[4:5], v[30:31]
	v_cvt_f64_f32_e32 v[4:5], v32
	v_fmac_f64_e32 v[38:39], v[46:47], v[4:5]
	v_cvt_f64_f32_e32 v[4:5], v33
	v_fmac_f64_e32 v[38:39], v[48:49], v[4:5]
	v_cvt_f64_f32_e32 v[4:5], v82
	v_cndmask_b32_e64 v5, 0, v5, s[26:27]
	v_cndmask_b32_e64 v4, 0, v4, s[26:27]
	v_cvt_f64_f32_e32 v[30:31], v26
	v_fmac_f64_e32 v[38:39], v[4:5], v[30:31]
	v_cvt_f64_f32_e32 v[4:5], v83
	v_cndmask_b32_e64 v5, 0, v5, s[26:27]
	v_cndmask_b32_e64 v4, 0, v4, s[26:27]
	v_cvt_f64_f32_e32 v[26:27], v27
	v_fmac_f64_e32 v[38:39], v[4:5], v[26:27]
	v_cvt_f64_f32_e32 v[4:5], v78
	v_cndmask_b32_e64 v5, 0, v5, s[28:29]
	v_cndmask_b32_e64 v4, 0, v4, s[28:29]
	v_cvt_f64_f32_e32 v[26:27], v28
	v_fmac_f64_e32 v[38:39], v[4:5], v[26:27]
	v_cvt_f64_f32_e32 v[4:5], v79
	v_cndmask_b32_e64 v5, 0, v5, s[28:29]
	v_cndmask_b32_e64 v4, 0, v4, s[28:29]
	v_cvt_f64_f32_e32 v[26:27], v29
	v_fmac_f64_e32 v[38:39], v[4:5], v[26:27]
	v_cvt_f64_f32_e32 v[4:5], v74
	v_cndmask_b32_e64 v5, 0, v5, s[22:23]
	v_cndmask_b32_e64 v4, 0, v4, s[22:23]
	v_cvt_f64_f32_e32 v[26:27], v22
	v_fmac_f64_e32 v[38:39], v[4:5], v[26:27]
	v_cvt_f64_f32_e32 v[4:5], v75
	v_cndmask_b32_e64 v5, 0, v5, s[22:23]
	v_cndmask_b32_e64 v4, 0, v4, s[22:23]
	v_cvt_f64_f32_e32 v[22:23], v23
	v_fmac_f64_e32 v[38:39], v[4:5], v[22:23]
	v_cvt_f64_f32_e32 v[4:5], v86
	v_cndmask_b32_e64 v5, 0, v5, s[24:25]
	v_cndmask_b32_e64 v4, 0, v4, s[24:25]
	v_cvt_f64_f32_e32 v[22:23], v24
	v_fmac_f64_e32 v[38:39], v[4:5], v[22:23]
	v_cvt_f64_f32_e32 v[4:5], v87
	v_cndmask_b32_e64 v5, 0, v5, s[24:25]
	v_cndmask_b32_e64 v4, 0, v4, s[24:25]
	v_cvt_f64_f32_e32 v[22:23], v25
	v_fmac_f64_e32 v[38:39], v[4:5], v[22:23]
	v_cvt_f64_f32_e32 v[4:5], v72
	v_cndmask_b32_e64 v5, 0, v5, s[20:21]
	v_cndmask_b32_e64 v4, 0, v4, s[20:21]
	v_cvt_f64_f32_e32 v[22:23], v18
	v_fma_f64 v[22:23], v[4:5], v[22:23], 0
	v_cvt_f64_f32_e32 v[4:5], v73
	v_cndmask_b32_e64 v5, 0, v5, s[20:21]
	v_cndmask_b32_e64 v4, 0, v4, s[20:21]
	v_cvt_f64_f32_e32 v[18:19], v19
	v_fmac_f64_e32 v[22:23], v[4:5], v[18:19]
	v_cvt_f64_f32_e32 v[4:5], v68
	v_cndmask_b32_e64 v5, 0, v5, s[14:15]
	v_cndmask_b32_e64 v4, 0, v4, s[14:15]
	v_cvt_f64_f32_e32 v[18:19], v20
	v_fmac_f64_e32 v[22:23], v[4:5], v[18:19]
	v_cvt_f64_f32_e32 v[4:5], v69
	v_cndmask_b32_e64 v5, 0, v5, s[14:15]
	v_cndmask_b32_e64 v4, 0, v4, s[14:15]
	v_cvt_f64_f32_e32 v[18:19], v21
	v_fmac_f64_e32 v[22:23], v[4:5], v[18:19]
	v_cvt_f64_f32_e32 v[4:5], v64
	v_cndmask_b32_e64 v5, 0, v5, s[10:11]
	v_cndmask_b32_e64 v4, 0, v4, s[10:11]
	v_cvt_f64_f32_e32 v[18:19], v14
	v_fmac_f64_e32 v[22:23], v[4:5], v[18:19]
	v_cvt_f64_f32_e32 v[4:5], v65
	v_cndmask_b32_e64 v5, 0, v5, s[10:11]
	v_cndmask_b32_e64 v4, 0, v4, s[10:11]
	v_cvt_f64_f32_e32 v[14:15], v15
	v_fmac_f64_e32 v[22:23], v[4:5], v[14:15]
	v_cvt_f64_f32_e32 v[4:5], v60
	v_cndmask_b32_e64 v5, 0, v5, s[12:13]
	v_cndmask_b32_e64 v4, 0, v4, s[12:13]
	v_cvt_f64_f32_e32 v[14:15], v16
	v_fmac_f64_e32 v[22:23], v[4:5], v[14:15]
	v_cvt_f64_f32_e32 v[4:5], v61
	v_cndmask_b32_e64 v5, 0, v5, s[12:13]
	v_cndmask_b32_e64 v4, 0, v4, s[12:13]
	v_cvt_f64_f32_e32 v[14:15], v17
	v_fmac_f64_e32 v[22:23], v[4:5], v[14:15]
	v_cvt_f64_f32_e32 v[4:5], v10
	v_fmac_f64_e32 v[22:23], v[46:47], v[4:5]
	v_cvt_f64_f32_e32 v[4:5], v11
	v_fmac_f64_e32 v[22:23], v[48:49], v[4:5]
	v_cvt_f64_f32_e32 v[4:5], v66
	v_cndmask_b32_e64 v5, 0, v5, s[16:17]
	v_cndmask_b32_e64 v4, 0, v4, s[16:17]
	v_cvt_f64_f32_e32 v[10:11], v12
	v_fmac_f64_e32 v[22:23], v[4:5], v[10:11]
	v_cvt_f64_f32_e32 v[4:5], v67
	v_cndmask_b32_e64 v5, 0, v5, s[16:17]
	v_cndmask_b32_e64 v4, 0, v4, s[16:17]
	v_cvt_f64_f32_e32 v[10:11], v13
	v_fmac_f64_e32 v[22:23], v[4:5], v[10:11]
	v_cvt_f64_f32_e32 v[4:5], v62
	v_cndmask_b32_e64 v5, 0, v5, s[18:19]
	v_cndmask_b32_e64 v4, 0, v4, s[18:19]
	v_cvt_f64_f32_e32 v[10:11], v6
	v_fmac_f64_e32 v[22:23], v[4:5], v[10:11]
	v_cvt_f64_f32_e32 v[4:5], v63
	v_cndmask_b32_e64 v5, 0, v5, s[18:19]
	v_cndmask_b32_e64 v4, 0, v4, s[18:19]
	v_cvt_f64_f32_e32 v[6:7], v7
	v_fmac_f64_e32 v[22:23], v[4:5], v[6:7]
	v_cvt_f64_f32_e32 v[4:5], v58
	v_cndmask_b32_e64 v5, 0, v5, s[8:9]
	v_cndmask_b32_e64 v4, 0, v4, s[8:9]
	v_cvt_f64_f32_e32 v[6:7], v8
	v_fmac_f64_e32 v[22:23], v[4:5], v[6:7]
	v_cvt_f64_f32_e32 v[4:5], v59
	v_cndmask_b32_e64 v5, 0, v5, s[8:9]
	v_cndmask_b32_e64 v4, 0, v4, s[8:9]
	v_cvt_f64_f32_e32 v[6:7], v9
	v_fmac_f64_e32 v[22:23], v[4:5], v[6:7]
	v_cvt_f64_f32_e32 v[4:5], v70
	v_cndmask_b32_e64 v5, 0, v5, s[6:7]
	v_cndmask_b32_e64 v4, 0, v4, s[6:7]
	v_cvt_f64_f32_e32 v[6:7], v2
	v_add_u32_e32 v2, 0xf6d8, v128
	v_fmac_f64_e32 v[22:23], v[4:5], v[6:7]
	ds_read2_b64 v[4:7], v2 offset1:1
	ds_read_b64 v[10:11], v128 offset:63208
	v_cvt_f64_f32_e32 v[8:9], v71
	v_cndmask_b32_e64 v9, 0, v9, s[6:7]
	v_cndmask_b32_e64 v8, 0, v8, s[6:7]
	v_cvt_f64_f32_e32 v[2:3], v3
	v_fmac_f64_e32 v[22:23], v[8:9], v[2:3]
	s_waitcnt lgkmcnt(1)
	v_mul_f64 v[2:3], v[38:39], v[6:7]
	v_fmac_f64_e32 v[2:3], v[22:23], v[4:5]
	s_waitcnt lgkmcnt(0)
	v_fmac_f64_e32 v[2:3], v[92:93], v[10:11]
	s_nop 1
	v_mov_b32_dpp v4, v2 quad_perm:[1,0,3,2] row_mask:0xf bank_mask:0xf
	v_mov_b32_dpp v5, v3 quad_perm:[1,0,3,2] row_mask:0xf bank_mask:0xf
	s_waitcnt lgkmcnt(0)
	v_add_f64 v[2:3], v[2:3], v[4:5]
	s_nop 1
	v_mov_b32_dpp v4, v2 quad_perm:[2,3,0,1] row_mask:0xf bank_mask:0xf
	v_mov_b32_dpp v5, v3 quad_perm:[2,3,0,1] row_mask:0xf bank_mask:0xf
	s_waitcnt lgkmcnt(0)
	v_add_f64 v[2:3], v[2:3], v[4:5]
	s_nop 1
	v_mov_b32_dpp v4, v2 row_half_mirror row_mask:0xf bank_mask:0xf
	v_mov_b32_dpp v5, v3 row_half_mirror row_mask:0xf bank_mask:0xf
	s_waitcnt lgkmcnt(0)
	v_add_f64 v[2:3], v[2:3], v[4:5]
	s_nop 1
	v_mov_b32_dpp v4, v2 row_mirror row_mask:0xf bank_mask:0xf
	v_mov_b32_dpp v5, v3 row_mirror row_mask:0xf bank_mask:0xf
	s_waitcnt lgkmcnt(0)
	v_add_f64 v[2:3], v[2:3], v[4:5]
	ds_bpermute_b32 v4, v122, v2
	ds_bpermute_b32 v5, v122, v3
	s_waitcnt lgkmcnt(0)
	v_add_f64 v[2:3], v[2:3], v[4:5]
	ds_bpermute_b32 v4, v121, v2
	ds_bpermute_b32 v5, v121, v3
	s_and_saveexec_b64 s[0:1], s[42:43]
	s_cbranch_execz .LBB2_44
	s_waitcnt lgkmcnt(0)
	v_add_f64 v[2:3], v[2:3], v[4:5]
	ds_write_b64 v133, v[2:3]
	s_branch .LBB2_44

.LBB2_63:
	s_or_b64 exec, exec, s[6:7]
	s_nop 1
	v_mov_b32_dpp v4, v2 quad_perm:[1,0,3,2] row_mask:0xf bank_mask:0xf
	v_mov_b32_dpp v5, v3 quad_perm:[1,0,3,2] row_mask:0xf bank_mask:0xf
	s_waitcnt lgkmcnt(2)
	v_mov_b32_dpp v9, v6 quad_perm:[1,0,3,2] row_mask:0xf bank_mask:0xf
	v_mov_b32_e32 v7, v3
	v_mov_b32_e32 v8, v2
	s_waitcnt lgkmcnt(1)
	v_cmp_lt_f64_e64 s[6:7], v[2:3], v[4:5]
	v_cmp_nlt_f64_e32 vcc, v[2:3], v[4:5]
	s_and_saveexec_b64 s[8:9], vcc
	s_cbranch_execz .LBB2_65
	v_cmp_eq_f64_e32 vcc, v[2:3], v[4:5]
	s_waitcnt lgkmcnt(0)
	v_cmp_lt_i32_e64 s[0:1], v9, v6
	s_and_b64 s[0:1], vcc, s[0:1]
	s_andn2_b64 s[6:7], s[6:7], exec
	s_and_b64 s[0:1], s[0:1], exec
	s_or_b64 s[6:7], s[6:7], s[0:1]

.LBB2_67:
	s_or_b64 exec, exec, s[0:1]
	s_nop 1
	v_mov_b32_dpp v4, v8 quad_perm:[2,3,0,1] row_mask:0xf bank_mask:0xf
	v_mov_b32_dpp v5, v7 quad_perm:[2,3,0,1] row_mask:0xf bank_mask:0xf
	s_waitcnt lgkmcnt(2)
	v_mov_b32_dpp v9, v6 quad_perm:[2,3,0,1] row_mask:0xf bank_mask:0xf
	s_waitcnt lgkmcnt(1)
	v_cmp_lt_f64_e64 s[6:7], v[2:3], v[4:5]
	v_cmp_nlt_f64_e32 vcc, v[2:3], v[4:5]
	s_and_saveexec_b64 s[8:9], vcc
	s_cbranch_execz .LBB2_69
	v_cmp_eq_f64_e32 vcc, v[2:3], v[4:5]
	s_waitcnt lgkmcnt(0)
	v_cmp_lt_i32_e64 s[0:1], v9, v6
	s_and_b64 s[0:1], vcc, s[0:1]
	s_andn2_b64 s[6:7], s[6:7], exec
	s_and_b64 s[0:1], s[0:1], exec
	s_or_b64 s[6:7], s[6:7], s[0:1]

.LBB2_71:
	s_or_b64 exec, exec, s[0:1]
	s_nop 1
	v_mov_b32_dpp v4, v8 row_half_mirror row_mask:0xf bank_mask:0xf
	v_mov_b32_dpp v5, v7 row_half_mirror row_mask:0xf bank_mask:0xf
	s_waitcnt lgkmcnt(2)
	v_mov_b32_dpp v9, v6 row_half_mirror row_mask:0xf bank_mask:0xf
	s_waitcnt lgkmcnt(1)
	v_cmp_lt_f64_e64 s[6:7], v[2:3], v[4:5]
	v_cmp_nlt_f64_e32 vcc, v[2:3], v[4:5]
	s_and_saveexec_b64 s[8:9], vcc
	s_cbranch_execz .LBB2_73
	v_cmp_eq_f64_e32 vcc, v[2:3], v[4:5]
	s_waitcnt lgkmcnt(0)
	v_cmp_lt_i32_e64 s[0:1], v9, v6
	s_and_b64 s[0:1], vcc, s[0:1]
	s_andn2_b64 s[6:7], s[6:7], exec
	s_and_b64 s[0:1], s[0:1], exec
	s_or_b64 s[6:7], s[6:7], s[0:1]

.LBB2_75:
	s_or_b64 exec, exec, s[0:1]
	s_nop 1
	v_mov_b32_dpp v4, v8 row_mirror row_mask:0xf bank_mask:0xf
	v_mov_b32_dpp v5, v7 row_mirror row_mask:0xf bank_mask:0xf
	s_waitcnt lgkmcnt(2)
	v_mov_b32_dpp v9, v6 row_mirror row_mask:0xf bank_mask:0xf
	s_waitcnt lgkmcnt(1)
	v_cmp_lt_f64_e64 s[6:7], v[2:3], v[4:5]
	v_cmp_nlt_f64_e32 vcc, v[2:3], v[4:5]
	s_and_saveexec_b64 s[8:9], vcc
	s_cbranch_execz .LBB2_77
	v_cmp_eq_f64_e32 vcc, v[2:3], v[4:5]
	s_waitcnt lgkmcnt(0)
	v_cmp_lt_i32_e64 s[0:1], v9, v6
	s_and_b64 s[0:1], vcc, s[0:1]
	s_andn2_b64 s[6:7], s[6:7], exec
	s_and_b64 s[0:1], s[0:1], exec
	s_or_b64 s[6:7], s[6:7], s[0:1]

.LBB2_110:
	s_or_b64 exec, exec, s[0:1]
	v_bfe_u32 v65, v0, 6, 1
	v_bfe_u32 v1, v0, 3, 1
	v_lshl_or_b32 v46, v65, 1, v1
	v_lshrrev_b32_e32 v1, 3, v0
	v_and_b32_e32 v97, 15, v0
	v_and_b32_e32 v1, 48, v1
	v_or_b32_e32 v63, v1, v97
	v_mul_lo_u16_e32 v2, 20, v63
	v_lshrrev_b16_e32 v2, 7, v2
	v_and_b32_e32 v2, 14, v2
	v_or_b32_e32 v110, 64, v63
	v_add_u32_sdwa v6, v63, v2 dst_sel:DWORD dst_unused:UNUSED_PAD src0_sel:DWORD src1_sel:WORD_0
	v_mul_lo_u16_e32 v2, 0x4f, v110
	v_lshrrev_b16_e32 v2, 9, v2
	v_and_b32_e32 v2, 62, v2
	v_bfe_u32 v62, v0, 4, 2
	v_and_b32_e32 v47, 7, v0
	v_add_u32_e32 v10, v110, v2
	v_lshl_add_u32 v84, v62, 4, 0
	v_mad_u32_u24 v2, v46, 10, v47
	s_movk_i32 s0, 0x110
	s_waitcnt vmcnt(0)
	v_mad_u32_u24 v34, v2, s0, v84
	s_waitcnt lgkmcnt(0)
	s_barrier
	ds_read_b128 v[2:5], v34 offset:61200
	v_or_b32_e32 v64, 0x80, v63
	v_min_u32_e32 v22, 0xa8, v64
	v_mul_lo_u16_e32 v7, 0x4f, v22
	v_mad_u32_u24 v98, v6, s0, v84
	v_lshrrev_b16_e32 v23, 9, v7
	ds_read_b128 v[6:9], v98
	v_mad_u32_u24 v111, v10, s0, v84
	ds_read_b128 v[10:13], v111
	ds_read_b128 v[14:17], v34 offset:61264
	ds_read_b128 v[18:21], v98 offset:64
	v_and_b32_e32 v23, 30, v23
	s_waitcnt lgkmcnt(3)
	v_mfma_f32_16x16x32_f16 v[6:9], v[2:5], v[6:9], 0
	v_add_u32_e32 v26, v22, v23
	v_mad_u32_u24 v117, v26, s0, v84
	ds_read_b128 v[22:25], v111 offset:64
	ds_read_b128 v[26:29], v117
	ds_read_b128 v[30:33], v117 offset:64
	s_waitcnt lgkmcnt(3)
	v_mfma_f32_16x16x32_f16 v[6:9], v[14:17], v[18:21], v[6:9]
	ds_read_b128 v[18:21], v34 offset:61328
	v_add_u32_e32 v58, 1, v47
	v_add_u32_e32 v85, 2, v47
	v_mfma_f32_16x16x32_f16 v[10:13], v[2:5], v[10:13], 0
	v_lshl_or_b32 v86, s2, 9, v0
	v_ashrrev_i32_e32 v87, 31, v86
	v_lshlrev_b64 v[74:75], 4, v[86:87]
	s_waitcnt lgkmcnt(2)
	v_mfma_f32_16x16x32_f16 v[2:5], v[2:5], v[26:29], 0
	v_mad_u32_u24 v90, v46, 10, 20
	v_lshl_add_u64 v[70:71], s[60:61], 0, v[74:75]
	v_add_co_u32_e32 v42, vcc, 0x200000, v70
	v_mfma_f32_16x16x32_f16 v[10:13], v[14:17], v[22:25], v[10:13]
	s_nop 0
	v_addc_co_u32_e32 v43, vcc, 0, v71, vcc
	v_add_co_u32_e32 v50, vcc, 0x400000, v70
	s_waitcnt lgkmcnt(1)
	v_mfma_f32_16x16x32_f16 v[2:5], v[14:17], v[30:33], v[2:5]
	ds_read_b128 v[14:17], v98 offset:128
	ds_read_b128 v[22:25], v34 offset:61392
	ds_read_b128 v[26:29], v98 offset:192
	v_addc_co_u32_e32 v51, vcc, 0, v71, vcc
	s_waitcnt lgkmcnt(2)
	v_mfma_f32_16x16x32_f16 v[6:9], v[18:21], v[14:17], v[6:9]
	ds_read_b128 v[14:17], v111 offset:128
	ds_read_b128 v[30:33], v111 offset:192
	v_add_co_u32_e32 v52, vcc, 0x600000, v70
	s_waitcnt lgkmcnt(1)
	v_mfma_f32_16x16x32_f16 v[10:13], v[18:21], v[14:17], v[10:13]
	ds_read_b128 v[14:17], v117 offset:128
	ds_read_b128 v[34:37], v117 offset:192
	v_addc_co_u32_e32 v53, vcc, 0, v71, vcc
	s_waitcnt lgkmcnt(1)
	v_mfma_f32_16x16x32_f16 v[2:5], v[18:21], v[14:17], v[2:5]
	v_mad_u32_u24 v14, v46, 10, v58
	v_mad_u32_u24 v38, v14, s0, v84
	ds_read_b128 v[14:17], v38 offset:61200
	v_mfma_f32_16x16x32_f16 v[6:9], v[22:25], v[26:29], v[6:9]
	v_add_co_u32_e32 v54, vcc, 0x800000, v70
	s_mov_b32 s1, 0x200000
	v_mfma_f32_16x16x32_f16 v[10:13], v[22:25], v[30:33], v[10:13]
	v_addc_co_u32_e32 v55, vcc, 0, v71, vcc
	v_lshl_add_u64 v[82:83], s[62:63], 0, v[74:75]
	s_waitcnt lgkmcnt(1)
	v_mfma_f32_16x16x32_f16 v[2:5], v[22:25], v[34:37], v[2:5]
	ds_read_b128 v[18:21], v98 offset:272
	ds_read_b128 v[22:25], v38 offset:61264
	ds_read_b128 v[26:29], v98 offset:336
	s_mov_b32 s2, 0x400000
	s_mov_b32 s3, 0x600000
	s_waitcnt lgkmcnt(2)
	v_mfma_f32_16x16x32_f16 v[6:9], v[14:17], v[18:21], v[6:9]
	ds_read_b128 v[18:21], v111 offset:272
	ds_read_b128 v[30:33], v111 offset:336
	s_add_i32 s6, 0, 0x13890
	s_waitcnt lgkmcnt(1)
	v_mfma_f32_16x16x32_f16 v[10:13], v[14:17], v[18:21], v[10:13]
	ds_read_b128 v[18:21], v117 offset:272
	ds_read_b128 v[34:37], v117 offset:336
	s_waitcnt lgkmcnt(1)
	v_mfma_f32_16x16x32_f16 v[2:5], v[14:17], v[18:21], v[2:5]
	ds_read_b128 v[14:17], v38 offset:61328
	v_mfma_f32_16x16x32_f16 v[6:9], v[22:25], v[26:29], v[6:9]
	v_mfma_f32_16x16x32_f16 v[10:13], v[22:25], v[30:33], v[10:13]
	s_waitcnt lgkmcnt(1)
	v_mfma_f32_16x16x32_f16 v[2:5], v[22:25], v[34:37], v[2:5]
	ds_read_b128 v[18:21], v98 offset:400
	ds_read_b128 v[22:25], v38 offset:61392
	ds_read_b128 v[26:29], v98 offset:464
	s_waitcnt lgkmcnt(2)
	v_mfma_f32_16x16x32_f16 v[6:9], v[14:17], v[18:21], v[6:9]
	ds_read_b128 v[18:21], v111 offset:400
	ds_read_b128 v[30:33], v111 offset:464
	s_waitcnt lgkmcnt(1)
	v_mfma_f32_16x16x32_f16 v[10:13], v[14:17], v[18:21], v[10:13]
	ds_read_b128 v[18:21], v117 offset:400
	ds_read_b128 v[34:37], v117 offset:464
	s_waitcnt lgkmcnt(1)
	v_mfma_f32_16x16x32_f16 v[2:5], v[14:17], v[18:21], v[2:5]
	v_mad_u32_u24 v14, v46, 10, v85
	v_mad_u32_u24 v38, v14, s0, v84
	ds_read_b128 v[14:17], v38 offset:61200
	v_mfma_f32_16x16x32_f16 v[6:9], v[22:25], v[26:29], v[6:9]
	v_mfma_f32_16x16x32_f16 v[10:13], v[22:25], v[30:33], v[10:13]
	s_waitcnt lgkmcnt(1)
	v_mfma_f32_16x16x32_f16 v[2:5], v[22:25], v[34:37], v[2:5]
	ds_read_b128 v[18:21], v98 offset:544
	ds_read_b128 v[22:25], v38 offset:61264
	ds_read_b128 v[26:29], v98 offset:608
	s_waitcnt lgkmcnt(2)
	v_mfma_f32_16x16x32_f16 v[6:9], v[14:17], v[18:21], v[6:9]
	ds_read_b128 v[18:21], v111 offset:544
	ds_read_b128 v[30:33], v111 offset:608
	s_waitcnt lgkmcnt(1)
	v_mfma_f32_16x16x32_f16 v[10:13], v[14:17], v[18:21], v[10:13]
	ds_read_b128 v[18:21], v117 offset:544
	ds_read_b128 v[34:37], v117 offset:608
	s_waitcnt lgkmcnt(1)
	v_mfma_f32_16x16x32_f16 v[2:5], v[14:17], v[18:21], v[2:5]
	ds_read_b128 v[14:17], v38 offset:61328
	v_mfma_f32_16x16x32_f16 v[6:9], v[22:25], v[26:29], v[6:9]
	v_mfma_f32_16x16x32_f16 v[10:13], v[22:25], v[30:33], v[10:13]
	s_waitcnt lgkmcnt(1)
	v_mfma_f32_16x16x32_f16 v[2:5], v[22:25], v[34:37], v[2:5]
	ds_read_b128 v[18:21], v98 offset:672
	ds_read_b128 v[22:25], v38 offset:61392
	ds_read_b128 v[26:29], v98 offset:736
	v_mad_u32_u24 v38, v46, 10, 10
	s_waitcnt lgkmcnt(2)
	v_mfma_f32_16x16x32_f16 v[6:9], v[14:17], v[18:21], v[6:9]
	ds_read_b128 v[18:21], v111 offset:672
	ds_read_b128 v[30:33], v111 offset:736
	s_waitcnt lgkmcnt(1)
	v_mfma_f32_16x16x32_f16 v[10:13], v[14:17], v[18:21], v[10:13]
	ds_read_b128 v[18:21], v117 offset:672
	ds_read_b128 v[34:37], v117 offset:736
	s_waitcnt lgkmcnt(1)
	v_mfma_f32_16x16x32_f16 v[2:5], v[14:17], v[18:21], v[2:5]
	v_add_u32_e32 v14, v47, v38
	v_mad_u32_u24 v39, v14, s0, v84
	ds_read_b128 v[14:17], v39 offset:61200
	v_mfma_f32_16x16x32_f16 v[6:9], v[22:25], v[26:29], v[6:9]
	v_mfma_f32_16x16x32_f16 v[10:13], v[22:25], v[30:33], v[10:13]
	s_waitcnt lgkmcnt(1)
	v_mfma_f32_16x16x32_f16 v[2:5], v[22:25], v[34:37], v[2:5]
	ds_read_b128 v[18:21], v98 offset:4080
	ds_read_b128 v[22:25], v39 offset:61264
	ds_read_b128 v[26:29], v98 offset:4144
	s_waitcnt lgkmcnt(2)
	v_mfma_f32_16x16x32_f16 v[6:9], v[14:17], v[18:21], v[6:9]
	ds_read_b128 v[18:21], v111 offset:4080
	ds_read_b128 v[30:33], v111 offset:4144
	s_waitcnt lgkmcnt(1)
	v_mfma_f32_16x16x32_f16 v[10:13], v[14:17], v[18:21], v[10:13]
	ds_read_b128 v[18:21], v117 offset:4080
	ds_read_b128 v[34:37], v117 offset:4144
	s_waitcnt lgkmcnt(1)
	v_mfma_f32_16x16x32_f16 v[2:5], v[14:17], v[18:21], v[2:5]
	ds_read_b128 v[14:17], v39 offset:61328
	v_mfma_f32_16x16x32_f16 v[6:9], v[22:25], v[26:29], v[6:9]
	v_mfma_f32_16x16x32_f16 v[10:13], v[22:25], v[30:33], v[10:13]
	s_waitcnt lgkmcnt(1)
	v_mfma_f32_16x16x32_f16 v[2:5], v[22:25], v[34:37], v[2:5]
	ds_read_b128 v[18:21], v98 offset:4208
	ds_read_b128 v[22:25], v39 offset:61392
	ds_read_b128 v[26:29], v98 offset:4272
	s_waitcnt lgkmcnt(2)
	v_mfma_f32_16x16x32_f16 v[6:9], v[14:17], v[18:21], v[6:9]
	ds_read_b128 v[18:21], v111 offset:4208
	ds_read_b128 v[30:33], v111 offset:4272
	s_waitcnt lgkmcnt(1)
	v_mfma_f32_16x16x32_f16 v[10:13], v[14:17], v[18:21], v[10:13]
	ds_read_b128 v[18:21], v117 offset:4208
	ds_read_b128 v[34:37], v117 offset:4272
	s_waitcnt lgkmcnt(1)
	v_mfma_f32_16x16x32_f16 v[2:5], v[14:17], v[18:21], v[2:5]
	v_add_u32_e32 v14, v58, v38
	v_mad_u32_u24 v39, v14, s0, v84
	ds_read_b128 v[14:17], v39 offset:61200
	v_mfma_f32_16x16x32_f16 v[6:9], v[22:25], v[26:29], v[6:9]
	v_mfma_f32_16x16x32_f16 v[10:13], v[22:25], v[30:33], v[10:13]
	s_waitcnt lgkmcnt(1)
	v_mfma_f32_16x16x32_f16 v[2:5], v[22:25], v[34:37], v[2:5]
	ds_read_b128 v[18:21], v98 offset:4352
	ds_read_b128 v[22:25], v39 offset:61264
	ds_read_b128 v[26:29], v98 offset:4416
	s_waitcnt lgkmcnt(2)
	v_mfma_f32_16x16x32_f16 v[6:9], v[14:17], v[18:21], v[6:9]
	ds_read_b128 v[18:21], v111 offset:4352
	ds_read_b128 v[30:33], v111 offset:4416
	s_waitcnt lgkmcnt(1)
	v_mfma_f32_16x16x32_f16 v[10:13], v[14:17], v[18:21], v[10:13]
	ds_read_b128 v[18:21], v117 offset:4352
	ds_read_b128 v[34:37], v117 offset:4416
	s_waitcnt lgkmcnt(1)
	v_mfma_f32_16x16x32_f16 v[2:5], v[14:17], v[18:21], v[2:5]
	ds_read_b128 v[14:17], v39 offset:61328
	v_mfma_f32_16x16x32_f16 v[6:9], v[22:25], v[26:29], v[6:9]
	v_mfma_f32_16x16x32_f16 v[10:13], v[22:25], v[30:33], v[10:13]
	s_waitcnt lgkmcnt(1)
	v_mfma_f32_16x16x32_f16 v[2:5], v[22:25], v[34:37], v[2:5]
	ds_read_b128 v[18:21], v98 offset:4480
	ds_read_b128 v[22:25], v39 offset:61392
	ds_read_b128 v[26:29], v98 offset:4544
	s_waitcnt lgkmcnt(2)
	v_mfma_f32_16x16x32_f16 v[6:9], v[14:17], v[18:21], v[6:9]
	ds_read_b128 v[18:21], v111 offset:4480
	ds_read_b128 v[30:33], v111 offset:4544
	s_waitcnt lgkmcnt(1)
	v_mfma_f32_16x16x32_f16 v[10:13], v[14:17], v[18:21], v[10:13]
	ds_read_b128 v[18:21], v117 offset:4480
	ds_read_b128 v[34:37], v117 offset:4544
	s_waitcnt lgkmcnt(1)
	v_mfma_f32_16x16x32_f16 v[2:5], v[14:17], v[18:21], v[2:5]
	v_add_u32_e32 v14, v85, v38
	v_mad_u32_u24 v38, v14, s0, v84
	ds_read_b128 v[14:17], v38 offset:61200
	v_mfma_f32_16x16x32_f16 v[6:9], v[22:25], v[26:29], v[6:9]
	v_mfma_f32_16x16x32_f16 v[10:13], v[22:25], v[30:33], v[10:13]
	s_waitcnt lgkmcnt(1)
	v_mfma_f32_16x16x32_f16 v[2:5], v[22:25], v[34:37], v[2:5]
	ds_read_b128 v[18:21], v98 offset:4624
	ds_read_b128 v[22:25], v38 offset:61264
	ds_read_b128 v[26:29], v98 offset:4688
	s_waitcnt lgkmcnt(2)
	v_mfma_f32_16x16x32_f16 v[6:9], v[14:17], v[18:21], v[6:9]
	ds_read_b128 v[18:21], v111 offset:4624
	ds_read_b128 v[30:33], v111 offset:4688
	s_waitcnt lgkmcnt(1)
	v_mfma_f32_16x16x32_f16 v[10:13], v[14:17], v[18:21], v[10:13]
	ds_read_b128 v[18:21], v117 offset:4624
	ds_read_b128 v[34:37], v117 offset:4688
	s_waitcnt lgkmcnt(1)
	v_mfma_f32_16x16x32_f16 v[2:5], v[14:17], v[18:21], v[2:5]
	ds_read_b128 v[14:17], v38 offset:61328
	ds_read_b128 v[18:21], v98 offset:4752
	v_mfma_f32_16x16x32_f16 v[6:9], v[22:25], v[26:29], v[6:9]
	v_mfma_f32_16x16x32_f16 v[10:13], v[22:25], v[30:33], v[10:13]
	s_waitcnt lgkmcnt(2)
	v_mfma_f32_16x16x32_f16 v[22:25], v[22:25], v[34:37], v[2:5]
	s_nop 2
	ds_read_b128 v[2:5], v111 offset:4752
	ds_read_b128 v[26:29], v38 offset:61392
	ds_read_b128 v[30:33], v98 offset:4816
	ds_read_b128 v[34:37], v117 offset:4752
	ds_read_b128 v[38:41], v111 offset:4816
	s_waitcnt lgkmcnt(5)
	v_mfma_f32_16x16x32_f16 v[18:21], v[14:17], v[18:21], v[6:9]
	s_waitcnt lgkmcnt(4)
	v_mfma_f32_16x16x32_f16 v[10:13], v[14:17], v[2:5], v[10:13]
	s_nop 0
	global_load_dwordx4 v[6:9], v[70:71], off nt
	global_load_dwordx4 v[2:5], v[42:43], off nt
	ds_read_b128 v[42:45], v117 offset:4816
	s_waitcnt lgkmcnt(2)
	v_mfma_f32_16x16x32_f16 v[14:17], v[14:17], v[34:37], v[22:25]
	s_nop 2
	v_add_u32_e32 v22, v47, v90
	v_mad_u32_u24 v56, v22, s0, v84
	ds_read_b128 v[22:25], v56 offset:61200
	v_mfma_f32_16x16x32_f16 v[18:21], v[26:29], v[30:33], v[18:21]
	ds_read_b128 v[30:33], v98 offset:8160
	s_waitcnt lgkmcnt(3)
	v_mfma_f32_16x16x32_f16 v[10:13], v[26:29], v[38:41], v[10:13]
	s_waitcnt lgkmcnt(2)
	v_mfma_f32_16x16x32_f16 v[14:17], v[26:29], v[42:45], v[14:17]
	ds_read_b128 v[26:29], v111 offset:8160
	ds_read_b128 v[34:37], v56 offset:61264
	ds_read_b128 v[38:41], v98 offset:8224
	s_waitcnt lgkmcnt(3)
	v_mfma_f32_16x16x32_f16 v[18:21], v[22:25], v[30:33], v[18:21]
	ds_read_b128 v[30:33], v117 offset:8160
	ds_read_b128 v[42:45], v111 offset:8224
	ds_read_b128 v[46:49], v117 offset:8224
	s_waitcnt lgkmcnt(5)
	v_mfma_f32_16x16x32_f16 v[26:29], v[22:25], v[26:29], v[10:13]
	s_waitcnt lgkmcnt(2)
	v_mfma_f32_16x16x32_f16 v[22:25], v[22:25], v[30:33], v[14:17]
	s_nop 2
	global_load_dwordx4 v[14:17], v[50:51], off nt
	global_load_dwordx4 v[10:13], v[52:53], off nt
	ds_read_b128 v[30:33], v56 offset:61328
	v_mfma_f32_16x16x32_f16 v[18:21], v[34:37], v[38:41], v[18:21]
	ds_read_b128 v[38:41], v98 offset:8288
	s_waitcnt lgkmcnt(3)
	v_mfma_f32_16x16x32_f16 v[26:29], v[34:37], v[42:45], v[26:29]
	s_waitcnt lgkmcnt(2)
	v_mfma_f32_16x16x32_f16 v[22:25], v[34:37], v[46:49], v[22:25]
	ds_read_b128 v[34:37], v111 offset:8288
	ds_read_b128 v[42:45], v56 offset:61392
	ds_read_b128 v[46:49], v98 offset:8352
	v_add_co_u32_e32 v56, vcc, 0xa00000, v70
	s_waitcnt lgkmcnt(3)
	v_mfma_f32_16x16x32_f16 v[38:41], v[30:33], v[38:41], v[18:21]
	s_nop 2
	ds_read_b128 v[18:21], v117 offset:8288
	ds_read_b128 v[50:53], v111 offset:8352
	v_addc_co_u32_e32 v57, vcc, 0, v71, vcc
	s_waitcnt lgkmcnt(2)
	v_mfma_f32_16x16x32_f16 v[38:41], v[42:45], v[46:49], v[38:41]
	v_add_u32_e32 v46, v58, v90
	v_mad_u32_u24 v80, v46, s0, v84
	v_add_co_u32_e32 v76, vcc, 0xc00000, v70
	v_mfma_f32_16x16x32_f16 v[26:29], v[30:33], v[34:37], v[26:29]
	ds_read_b128 v[34:37], v117 offset:8352
	v_addc_co_u32_e32 v77, vcc, 0, v71, vcc
	s_waitcnt lgkmcnt(2)
	v_mfma_f32_16x16x32_f16 v[30:33], v[30:33], v[18:21], v[22:25]
	s_nop 2
	global_load_dwordx4 v[22:25], v[54:55], off nt
	global_load_dwordx4 v[18:21], v[56:57], off nt
	ds_read_b128 v[46:49], v80 offset:61200
	v_add_co_u32_e32 v78, vcc, 0xe00000, v70
	s_waitcnt lgkmcnt(2)
	v_mfma_f32_16x16x32_f16 v[26:29], v[42:45], v[50:53], v[26:29]
	ds_read_b128 v[50:53], v98 offset:8432
	v_addc_co_u32_e32 v79, vcc, 0, v71, vcc
	s_waitcnt lgkmcnt(2)
	v_mfma_f32_16x16x32_f16 v[30:33], v[42:45], v[34:37], v[30:33]
	ds_read_b128 v[34:37], v111 offset:8432
	ds_read_b128 v[42:45], v80 offset:61264
	ds_read_b128 v[54:57], v98 offset:8496
	v_add_co_u32_e32 v74, vcc, s1, v82
	s_waitcnt lgkmcnt(3)
	v_mfma_f32_16x16x32_f16 v[38:41], v[46:49], v[50:53], v[38:41]
	ds_read_b128 v[50:53], v117 offset:8432
	ds_read_b128 v[58:61], v111 offset:8496
	ds_read_b128 v[70:73], v117 offset:8496
	v_addc_co_u32_e32 v75, vcc, 0, v83, vcc
	s_waitcnt lgkmcnt(5)
	v_mfma_f32_16x16x32_f16 v[66:69], v[46:49], v[34:37], v[26:29]
	global_load_dwordx4 v[34:37], v[76:77], off nt
	s_nop 1
	global_load_dwordx4 v[26:29], v[78:79], off nt
	v_add_co_u32_e32 v88, vcc, s2, v82
	s_waitcnt lgkmcnt(2)
	v_mfma_f32_16x16x32_f16 v[30:33], v[46:49], v[50:53], v[30:33]
	ds_read_b128 v[46:49], v80 offset:61328
	v_addc_co_u32_e32 v89, vcc, 0, v83, vcc
	v_mfma_f32_16x16x32_f16 v[38:41], v[42:45], v[54:57], v[38:41]
	ds_read_b128 v[54:57], v98 offset:8560
	s_movk_i32 s2, 0xa9
	s_waitcnt lgkmcnt(3)
	v_mfma_f32_16x16x32_f16 v[50:53], v[42:45], v[58:61], v[66:69]
	s_waitcnt lgkmcnt(2)
	v_mfma_f32_16x16x32_f16 v[42:45], v[42:45], v[70:73], v[30:33]
	ds_read_b128 v[58:61], v111 offset:8560
	ds_read_b128 v[66:69], v80 offset:61392
	ds_read_b128 v[70:73], v98 offset:8624
	s_waitcnt lgkmcnt(3)
	v_mfma_f32_16x16x32_f16 v[54:57], v[46:49], v[54:57], v[38:41]
	s_nop 2
	global_load_dwordx4 v[38:41], v[82:83], off nt
	global_load_dwordx4 v[30:33], v[74:75], off nt
	ds_read_b128 v[74:77], v117 offset:8560
	ds_read_b128 v[78:81], v111 offset:8624
	s_waitcnt lgkmcnt(4)
	v_mfma_f32_16x16x32_f16 v[50:53], v[46:49], v[58:61], v[50:53]
	ds_read_b128 v[58:61], v117 offset:8624
	s_waitcnt lgkmcnt(2)
	v_mfma_f32_16x16x32_f16 v[42:45], v[46:49], v[74:77], v[42:45]
	v_mfma_f32_16x16x32_f16 v[46:49], v[66:69], v[70:73], v[54:57]
	ds_read_b128 v[70:73], v98 offset:8704
	s_nop 1
	v_add_u32_e32 v54, v85, v90
	v_mad_u32_u24 v92, v54, s0, v84
	ds_read_b128 v[54:57], v92 offset:61200
	s_waitcnt lgkmcnt(3)
	v_mfma_f32_16x16x32_f16 v[50:53], v[66:69], v[78:81], v[50:53]
	v_add_co_u32_e32 v90, vcc, s3, v82
	s_add_i32 s0, 0, 0x13550
	s_waitcnt lgkmcnt(2)
	v_mfma_f32_16x16x32_f16 v[58:61], v[66:69], v[58:61], v[42:45]
	s_nop 2
	ds_read_b128 v[42:45], v111 offset:8704
	ds_read_b128 v[66:69], v92 offset:61264
	ds_read_b128 v[74:77], v98 offset:8768
	v_addc_co_u32_e32 v91, vcc, 0, v83, vcc
	s_waitcnt lgkmcnt(3)
	v_mfma_f32_16x16x32_f16 v[70:73], v[54:57], v[70:73], v[46:49]
	ds_read_b128 v[78:81], v117 offset:8704
	ds_read_b128 v[82:85], v111 offset:8768
	v_cmp_gt_u32_e64 s[2:3], s2, v64
	v_cmp_eq_u32_e32 vcc, 0, v97
	s_waitcnt lgkmcnt(4)
	v_mfma_f32_16x16x32_f16 v[50:53], v[54:57], v[42:45], v[50:53]
	global_load_dwordx4 v[46:49], v[88:89], off nt
	global_load_dwordx4 v[42:45], v[90:91], off nt
	ds_read_b128 v[88:91], v117 offset:8768
	s_waitcnt lgkmcnt(2)
	v_mfma_f32_16x16x32_f16 v[54:57], v[54:57], v[78:81], v[58:61]
	s_nop 2
	ds_read_b128 v[58:61], v92 offset:61328
	ds_read_b128 v[92:95], v92 offset:61392
	ds_read_b128 v[78:81], v98 offset:8832
	ds_read_b128 v[98:101], v98 offset:8896
	ds_read_b128 v[106:109], v111 offset:8832
	ds_read_b128 v[118:121], v111 offset:8896
	ds_read_b128 v[122:125], v117 offset:8832
	ds_read_b128 v[126:129], v117 offset:8896
	v_mfma_f32_16x16x32_f16 v[102:105], v[66:69], v[74:77], v[70:73]
	s_waitcnt lgkmcnt(9)
	v_mfma_f32_16x16x32_f16 v[50:53], v[66:69], v[82:85], v[50:53]
	s_nop 0
	v_lshlrev_b32_e32 v70, 2, v62
	v_lshl_or_b32 v73, v65, 4, v70
	v_lshl_add_u32 v75, v73, 2, 0
	s_waitcnt lgkmcnt(8)
	v_mfma_f32_16x16x32_f16 v[66:69], v[66:69], v[88:91], v[54:57]
	v_add_u32_e32 v65, 0x13810, v75
	v_min_u32_e32 v72, 0xaf, v64
	v_lshl_add_u32 v70, v63, 2, s0
	s_waitcnt lgkmcnt(5)
	v_mfma_f32_16x16x32_f16 v[54:57], v[58:61], v[78:81], v[102:105]
	v_lshl_add_u32 v71, v110, 2, s0
	v_lshl_add_u32 v72, v72, 2, s0
	ds_read_b32 v65, v65
	ds_read_b32 v79, v70
	ds_read_b32 v78, v71
	ds_read_b32 v77, v72
	s_waitcnt lgkmcnt(7)
	v_mfma_f32_16x16x32_f16 v[80:83], v[58:61], v[106:109], v[50:53]
	s_movk_i32 s0, 0x69
	v_cmp_gt_u32_e64 s[0:1], s0, v63
	s_waitcnt lgkmcnt(5)
	v_mfma_f32_16x16x32_f16 v[58:61], v[58:61], v[122:125], v[66:69]
	v_mfma_f32_16x16x32_f16 v[50:53], v[92:95], v[98:101], v[54:57]
	v_mfma_f32_16x16x32_f16 v[54:57], v[92:95], v[118:121], v[80:83]
	s_waitcnt lgkmcnt(4)
	v_mfma_f32_16x16x32_f16 v[58:61], v[92:95], v[126:129], v[58:61]
	s_waitcnt lgkmcnt(2)
	s_nop 3
	v_or_b32_e32 v69, 1, v73
	v_or_b32_e32 v64, 2, v73
	v_or_b32_e32 v152, 3, v73
	v_lshl_add_u32 v71, v69, 2, 0
	v_lshl_add_u32 v66, v64, 2, 0
	v_lshl_add_u32 v153, v152, 2, 0
	v_add_u32_e32 v160, 0x13810, v71
	v_add_u32_e32 v161, 0x13810, v66
	v_add_u32_e32 v162, 0x13810, v153
	ds_read_b32 v160, v160
	ds_read_b32 v161, v161
	ds_read_b32 v162, v162
	v_mov_b32_e32 v155, 0xff800000
	s_waitcnt lgkmcnt(3)
	v_mul_f32_e32 v164, v50, v79
	v_mul_f32_e32 v165, v54, v78
	v_mul_f32_e32 v166, v58, v77
	v_mul_f32_e32 v164, v65, v164
	v_mul_f32_e32 v165, v65, v165
	v_mul_f32_e32 v166, v65, v166
	v_mul_f32_e32 v167, v51, v79
	v_mul_f32_e32 v168, v55, v78
	v_mul_f32_e32 v169, v59, v77
	v_mul_f32_e32 v170, v52, v79
	v_mul_f32_e32 v171, v56, v78
	v_mul_f32_e32 v172, v60, v77
	v_mul_f32_e32 v173, v53, v79
	v_mul_f32_e32 v174, v57, v78
	v_mul_f32_e32 v175, v61, v77
	s_waitcnt lgkmcnt(0)
	v_mul_f32_e32 v167, v160, v167
	v_mul_f32_e32 v168, v160, v168
	v_mul_f32_e32 v169, v160, v169
	v_mul_f32_e32 v170, v161, v170
	v_mul_f32_e32 v171, v161, v171
	v_mul_f32_e32 v172, v161, v172
	v_mul_f32_e32 v173, v162, v173
	v_mul_f32_e32 v174, v162, v174
	v_mul_f32_e32 v175, v162, v175
	v_cndmask_b32_e64 v165, v155, v165, s[0:1]
	v_cndmask_b32_e64 v166, v155, v166, s[2:3]
	v_cndmask_b32_e64 v168, v155, v168, s[0:1]
	v_cndmask_b32_e64 v169, v155, v169, s[2:3]
	v_cndmask_b32_e64 v171, v155, v171, s[0:1]
	v_cndmask_b32_e64 v172, v155, v172, s[2:3]
	v_cndmask_b32_e64 v174, v155, v174, s[0:1]
	v_cndmask_b32_e64 v175, v155, v175, s[2:3]
	v_max_f32_e32 v176, 0xff800000, v164
	v_max_f32_e32 v177, 0xff800000, v167
	v_max_f32_e32 v178, 0xff800000, v170
	v_max_f32_e32 v179, 0xff800000, v173
	v_max3_f32 v176, v176, v165, v166
	v_max3_f32 v177, v177, v168, v169
	v_max3_f32 v178, v178, v171, v172
	v_max3_f32 v179, v179, v174, v175
	v_max_f32_dpp v176, v176, v176 quad_perm:[1,0,3,2] row_mask:0xf bank_mask:0xf
	v_max_f32_dpp v177, v177, v177 quad_perm:[1,0,3,2] row_mask:0xf bank_mask:0xf
	v_max_f32_dpp v178, v178, v178 quad_perm:[1,0,3,2] row_mask:0xf bank_mask:0xf
	v_max_f32_dpp v179, v179, v179 quad_perm:[1,0,3,2] row_mask:0xf bank_mask:0xf
	v_max_f32_dpp v176, v176, v176 quad_perm:[2,3,0,1] row_mask:0xf bank_mask:0xf
	v_max_f32_dpp v177, v177, v177 quad_perm:[2,3,0,1] row_mask:0xf bank_mask:0xf
	v_max_f32_dpp v178, v178, v178 quad_perm:[2,3,0,1] row_mask:0xf bank_mask:0xf
	v_max_f32_dpp v179, v179, v179 quad_perm:[2,3,0,1] row_mask:0xf bank_mask:0xf
	v_max_f32_dpp v176, v176, v176 row_half_mirror row_mask:0xf bank_mask:0xf
	v_max_f32_dpp v177, v177, v177 row_half_mirror row_mask:0xf bank_mask:0xf
	v_max_f32_dpp v178, v178, v178 row_half_mirror row_mask:0xf bank_mask:0xf
	v_max_f32_dpp v179, v179, v179 row_half_mirror row_mask:0xf bank_mask:0xf
	v_max_f32_dpp v176, v176, v176 row_mirror row_mask:0xf bank_mask:0xf
	v_max_f32_dpp v177, v177, v177 row_mirror row_mask:0xf bank_mask:0xf
	v_max_f32_dpp v178, v178, v178 row_mirror row_mask:0xf bank_mask:0xf
	v_max_f32_dpp v179, v179, v179 row_mirror row_mask:0xf bank_mask:0xf
	v_and_b32_e32 v58, 0x180, v0
	v_add_u32_e32 v58, s6, v58
	v_lshl_add_u32 v58, v73, 2, v58
	s_and_saveexec_b64 s[6:7], vcc
	ds_write_b128 v58, v[176:179]
	s_or_b64 exec, exec, s[6:7]
	v_mov_b32_e32 v76, v164
	v_mov_b32_e32 v74, v165
	v_mov_b32_e32 v72, v166
	v_mov_b32_e32 v70, v167
	v_mov_b32_e32 v68, v168
	v_mov_b32_e32 v67, v169
	v_mov_b32_e32 v65, v170
	v_mov_b32_e32 v59, v171
	v_mov_b32_e32 v56, v172
	v_mov_b32_e32 v53, v173
	v_mov_b32_e32 v52, v174
	v_mov_b32_e32 v50, v175
	v_mov_b32_e32 v54, v152
	v_mov_b32_e32 v55, v153
	v_add_u32_e32 v51, 0x13890, v75
	s_waitcnt lgkmcnt(0)
	s_barrier
	ds_read2_b32 v[60:61], v51 offset0:64 offset1:96
	ds_read2_b32 v[78:79], v51 offset1:32
	s_add_i32 s13, 0, 0x13a90
	s_waitcnt lgkmcnt(1)
	v_max_f32_e32 v51, v61, v61
	v_max_f32_e32 v57, v60, v60
	v_max_f32_e32 v51, v57, v51
	s_waitcnt lgkmcnt(0)
	v_max3_f32 v51, v78, v79, v51
	v_add_f32_e32 v75, 0xbb102de0, v51
	v_mad_u32_u24 v61, v73, 24, s13
	v_lshlrev_b32_e32 v60, 8, v73
	v_cmp_ge_f32_e64 s[0:1], v76, v75
	v_lshlrev_b32_e64 v57, v63, 1
	s_and_saveexec_b64 s[2:3], s[0:1]
	s_cbranch_execz .LBB2_122
	v_lshrrev_b32_e32 v51, 6, v0
	v_and_b32_e32 v51, 4, v51
	v_add_u32_e32 v51, v61, v51
	s_mov_b64 s[6:7], exec
	ds_or_b32 v51, v57
	v_mbcnt_lo_u32_b32 v51, s6, 0
	v_mbcnt_hi_u32_b32 v51, s7, v51
	v_cmp_eq_u32_e64 s[0:1], 0, v51
	s_and_saveexec_b64 s[8:9], s[0:1]
	s_bcnt1_i32_b64 s0, s[6:7]
	s_add_i32 s1, 0, 0x13d90
	v_mov_b32_e32 v58, s1
	v_mov_b32_e32 v76, s0
	ds_add_rtn_u32 v58, v58, v76
	s_or_b64 exec, exec, s[8:9]
	s_waitcnt lgkmcnt(0)
	v_readfirstlane_b32 s0, v58
	v_or_b32_e32 v58, v63, v60
	s_nop 0
	v_add_u32_e32 v51, s0, v51
	v_lshl_add_u32 v51, v51, 1, 0
	ds_write_b16 v51, v58

.LBB2_169:
	ds_read_u16 v0, v102
	s_waitcnt lgkmcnt(0)
	v_and_b32_e32 v105, 0xffff, v0
	v_mul_lo_u16_sdwa v0, v0, s6 dst_sel:DWORD dst_unused:UNUSED_PAD src0_sel:BYTE_0 src1_sel:DWORD
	v_lshrrev_b32_e32 v50, 11, v105
	v_bfe_u32 v54, v105, 8, 3
	v_lshrrev_b16_e32 v52, 10, v0
	v_and_b32_e32 v104, 0xff, v105
	v_add_u32_e32 v55, s12, v54
	v_mul_i32_i24_e32 v0, -13, v52
	v_add_u32_e32 v56, s11, v50
	v_add3_u32 v57, v104, v96, v0
	v_med3_i32 v0, v56, 0, 63
	v_med3_i32 v50, v55, 0, 63
	v_add_lshl_u32 v60, s10, v52, 6
	v_lshlrev_b32_e32 v58, 15, v0
	v_lshlrev_b32_e32 v59, 9, v50
	v_add_u32_e32 v52, v57, v60
	v_or_b32_e32 v0, v58, v59
	v_ashrrev_i32_e32 v53, 31, v52
	v_lshl_add_u64 v[50:51], v[88:89], 0, v[0:1]
	v_lshlrev_b64 v[52:53], 9, v[52:53]
	v_lshl_add_u64 v[52:53], v[90:91], 0, v[52:53]
	global_load_dwordx4 v[106:109], v[50:51], off offset:16
	global_load_dwordx4 v[70:73], v[50:51], off
	global_load_dwordx4 v[116:119], v[52:53], off offset:16
	global_load_dwordx4 v[120:123], v[52:53], off
	v_or_b32_e32 v0, s33, v54
	v_add_u32_e32 v61, 1, v57
	v_lshlrev_b32_e32 v54, 9, v0
	v_add_u32_e32 v52, v61, v60
	v_or_b32_e32 v0, v58, v54
	v_ashrrev_i32_e32 v53, 31, v52
	v_lshl_add_u64 v[50:51], v[88:89], 0, v[0:1]
	v_lshlrev_b64 v[52:53], 9, v[52:53]
	v_lshl_add_u64 v[52:53], v[90:91], 0, v[52:53]
	global_load_dwordx4 v[124:127], v[50:51], off offset:16
	global_load_dwordx4 v[128:131], v[50:51], off
	global_load_dwordx4 v[132:135], v[52:53], off offset:16
	global_load_dwordx4 v[136:139], v[52:53], off
	v_max_i32_e32 v0, -2, v55
	v_add_u32_e32 v0, 2, v0
	v_min_u32_e32 v0, 63, v0
	v_add_u32_e32 v64, 2, v57
	v_lshlrev_b32_e32 v62, 9, v0
	v_add_u32_e32 v52, v64, v60
	v_or_b32_e32 v0, v58, v62
	v_ashrrev_i32_e32 v53, 31, v52
	v_lshl_add_u64 v[50:51], v[88:89], 0, v[0:1]
	v_lshlrev_b64 v[52:53], 9, v[52:53]
	v_lshl_add_u64 v[52:53], v[90:91], 0, v[52:53]
	global_load_dwordx4 v[140:143], v[50:51], off offset:16
	global_load_dwordx4 v[144:147], v[50:51], off
	global_load_dwordx4 v[148:151], v[52:53], off offset:16
	global_load_dwordx4 v[152:155], v[52:53], off
	v_max_i32_e32 v0, -1, v56
	v_add_u32_e32 v0, 1, v0
	v_min_u32_e32 v0, 63, v0
	v_add_u32_e32 v58, 64, v60
	v_lshlrev_b32_e32 v55, 15, v0
	v_add_u32_e32 v52, v57, v58
	v_or_b32_e32 v0, v55, v59
	v_ashrrev_i32_e32 v53, 31, v52
	v_lshl_add_u64 v[50:51], v[88:89], 0, v[0:1]
	v_lshlrev_b64 v[52:53], 9, v[52:53]
	v_lshl_add_u64 v[52:53], v[90:91], 0, v[52:53]
	global_load_dwordx4 v[156:159], v[50:51], off offset:16
	global_load_dwordx4 v[160:163], v[50:51], off
	global_load_dwordx4 v[164:167], v[52:53], off offset:16
	global_load_dwordx4 v[168:171], v[52:53], off
	v_add_u32_e32 v52, v61, v58
	v_or_b32_e32 v0, v55, v54
	v_ashrrev_i32_e32 v53, 31, v52
	v_lshl_add_u64 v[50:51], v[88:89], 0, v[0:1]
	v_lshlrev_b64 v[52:53], 9, v[52:53]
	v_lshl_add_u64 v[52:53], v[90:91], 0, v[52:53]
	global_load_dwordx4 v[172:175], v[50:51], off offset:16
	global_load_dwordx4 v[176:179], v[50:51], off
	global_load_dwordx4 v[180:183], v[52:53], off offset:16
	global_load_dwordx4 v[184:187], v[52:53], off
	v_add_u32_e32 v52, v64, v58
	v_or_b32_e32 v0, v55, v62
	v_ashrrev_i32_e32 v53, 31, v52
	v_lshl_add_u64 v[50:51], v[88:89], 0, v[0:1]
	v_lshlrev_b64 v[52:53], 9, v[52:53]
	v_lshl_add_u64 v[52:53], v[90:91], 0, v[52:53]
	global_load_dwordx4 v[188:191], v[50:51], off offset:16
	global_load_dwordx4 v[192:195], v[50:51], off
	global_load_dwordx4 v[196:199], v[52:53], off offset:16
	global_load_dwordx4 v[200:203], v[52:53], off
	v_max_i32_e32 v0, -2, v56
	v_add_u32_e32 v0, 2, v0
	v_min_u32_e32 v0, 63, v0
	v_add_u32_e32 v65, 0x80, v60
	v_lshlrev_b32_e32 v63, 15, v0
	v_add_u32_e32 v52, v57, v65
	v_or_b32_e32 v0, v63, v59
	v_ashrrev_i32_e32 v53, 31, v52
	v_lshl_add_u64 v[50:51], v[88:89], 0, v[0:1]
	v_lshlrev_b64 v[52:53], 9, v[52:53]
	v_lshl_add_u64 v[52:53], v[90:91], 0, v[52:53]
	global_load_dwordx4 v[74:77], v[50:51], off offset:16
	global_load_dwordx4 v[204:207], v[50:51], off
	global_load_dwordx4 v[82:85], v[52:53], off offset:16
	global_load_dwordx4 v[208:211], v[52:53], off
	v_add_u32_e32 v52, v61, v65
	v_or_b32_e32 v0, v63, v54
	v_ashrrev_i32_e32 v53, 31, v52
	v_lshl_add_u64 v[50:51], v[88:89], 0, v[0:1]
	v_lshlrev_b64 v[52:53], 9, v[52:53]
	v_lshl_add_u64 v[52:53], v[90:91], 0, v[52:53]
	global_load_dwordx4 v[54:57], v[50:51], off offset:16
	global_load_dwordx4 v[66:69], v[50:51], off
	global_load_dwordx4 v[58:61], v[52:53], off offset:16
	global_load_dwordx4 v[78:81], v[52:53], off
	v_add_u32_e32 v50, v64, v65
	v_ashrrev_i32_e32 v51, 31, v50
	v_lshlrev_b64 v[50:51], 9, v[50:51]
	v_lshl_add_u64 v[110:111], v[90:91], 0, v[50:51]
	v_or_b32_e32 v0, v63, v62
	v_lshl_add_u64 v[62:63], v[88:89], 0, v[0:1]
	s_waitcnt vmcnt(30)
	v_cvt_f64_f32_e32 v[50:51], v70
	s_waitcnt vmcnt(28)
	v_cvt_f64_f32_e32 v[52:53], v120
	v_fma_f64 v[92:93], v[50:51], v[52:53], 0
	v_cvt_f64_f32_e32 v[50:51], v72
	v_cvt_f64_f32_e32 v[52:53], v122
	v_fmac_f64_e32 v[92:93], v[50:51], v[52:53]
	v_cvt_f64_f32_e32 v[50:51], v71
	v_cvt_f64_f32_e32 v[52:53], v121
	v_fma_f64 v[94:95], v[50:51], v[52:53], 0
	v_cvt_f64_f32_e32 v[70:71], v73
	v_cvt_f64_f32_e32 v[72:73], v123
	v_fmac_f64_e32 v[94:95], v[70:71], v[72:73]
	v_cvt_f64_f32_e32 v[70:71], v106
	v_cvt_f64_f32_e32 v[72:73], v116
	v_fmac_f64_e32 v[92:93], v[70:71], v[72:73]
	v_cvt_f64_f32_e32 v[70:71], v107
	v_cvt_f64_f32_e32 v[72:73], v117
	v_fmac_f64_e32 v[94:95], v[70:71], v[72:73]
	v_cvt_f64_f32_e32 v[70:71], v108
	v_cvt_f64_f32_e32 v[72:73], v118
	global_load_dwordx4 v[50:53], v[62:63], off offset:16
	s_nop 0
	global_load_dwordx4 v[62:65], v[62:63], off
	v_fmac_f64_e32 v[92:93], v[70:71], v[72:73]
	global_load_dwordx4 v[70:73], v[110:111], off offset:16
	global_load_dwordx4 v[120:123], v[110:111], off
	v_cvt_f64_f32_e32 v[106:107], v109
	v_cvt_f64_f32_e32 v[108:109], v119
	v_fmac_f64_e32 v[94:95], v[106:107], v[108:109]
	s_waitcnt vmcnt(30)
	v_cvt_f64_f32_e32 v[106:107], v128
	s_waitcnt vmcnt(28)
	v_cvt_f64_f32_e32 v[108:109], v136
	v_fmac_f64_e32 v[92:93], v[106:107], v[108:109]
	v_cvt_f64_f32_e32 v[106:107], v129
	v_cvt_f64_f32_e32 v[108:109], v137
	v_fmac_f64_e32 v[94:95], v[106:107], v[108:109]
	v_cvt_f64_f32_e32 v[106:107], v130
	v_cvt_f64_f32_e32 v[108:109], v138
	v_fmac_f64_e32 v[92:93], v[106:107], v[108:109]
	v_cvt_f64_f32_e32 v[106:107], v131
	v_cvt_f64_f32_e32 v[108:109], v139
	v_fmac_f64_e32 v[94:95], v[106:107], v[108:109]
	v_cvt_f64_f32_e32 v[106:107], v124
	v_cvt_f64_f32_e32 v[108:109], v132
	v_fmac_f64_e32 v[92:93], v[106:107], v[108:109]
	v_cvt_f64_f32_e32 v[106:107], v125
	v_cvt_f64_f32_e32 v[108:109], v133
	v_fmac_f64_e32 v[94:95], v[106:107], v[108:109]
	v_cvt_f64_f32_e32 v[106:107], v126
	v_cvt_f64_f32_e32 v[108:109], v134
	v_fmac_f64_e32 v[92:93], v[106:107], v[108:109]
	v_cvt_f64_f32_e32 v[106:107], v127
	v_cvt_f64_f32_e32 v[108:109], v135
	v_fmac_f64_e32 v[94:95], v[106:107], v[108:109]
	s_waitcnt vmcnt(26)
	v_cvt_f64_f32_e32 v[106:107], v144
	s_waitcnt vmcnt(24)
	v_cvt_f64_f32_e32 v[108:109], v152
	v_fmac_f64_e32 v[92:93], v[106:107], v[108:109]
	v_cvt_f64_f32_e32 v[106:107], v145
	v_cvt_f64_f32_e32 v[108:109], v153
	v_fmac_f64_e32 v[94:95], v[106:107], v[108:109]
	v_cvt_f64_f32_e32 v[106:107], v146
	v_cvt_f64_f32_e32 v[108:109], v154
	v_fmac_f64_e32 v[92:93], v[106:107], v[108:109]
	v_cvt_f64_f32_e32 v[106:107], v147
	v_cvt_f64_f32_e32 v[108:109], v155
	v_fmac_f64_e32 v[94:95], v[106:107], v[108:109]
	v_cvt_f64_f32_e32 v[106:107], v140
	v_cvt_f64_f32_e32 v[108:109], v148
	v_fmac_f64_e32 v[92:93], v[106:107], v[108:109]
	v_cvt_f64_f32_e32 v[106:107], v141
	v_cvt_f64_f32_e32 v[108:109], v149
	v_fmac_f64_e32 v[94:95], v[106:107], v[108:109]
	v_cvt_f64_f32_e32 v[106:107], v142
	v_cvt_f64_f32_e32 v[108:109], v150
	v_fmac_f64_e32 v[92:93], v[106:107], v[108:109]
	v_cvt_f64_f32_e32 v[106:107], v143
	v_cvt_f64_f32_e32 v[108:109], v151
	v_fmac_f64_e32 v[94:95], v[106:107], v[108:109]
	s_waitcnt vmcnt(22)
	v_cvt_f64_f32_e32 v[106:107], v160
	s_waitcnt vmcnt(20)
	v_cvt_f64_f32_e32 v[108:109], v168
	v_fmac_f64_e32 v[92:93], v[106:107], v[108:109]
	v_cvt_f64_f32_e32 v[106:107], v161
	v_cvt_f64_f32_e32 v[108:109], v169
	v_fmac_f64_e32 v[94:95], v[106:107], v[108:109]
	v_cvt_f64_f32_e32 v[106:107], v162
	v_cvt_f64_f32_e32 v[108:109], v170
	v_fmac_f64_e32 v[92:93], v[106:107], v[108:109]
	v_cvt_f64_f32_e32 v[106:107], v163
	v_cvt_f64_f32_e32 v[108:109], v171
	v_fmac_f64_e32 v[94:95], v[106:107], v[108:109]
	v_cvt_f64_f32_e32 v[106:107], v156
	v_cvt_f64_f32_e32 v[108:109], v164
	v_fmac_f64_e32 v[92:93], v[106:107], v[108:109]
	v_cvt_f64_f32_e32 v[106:107], v157
	v_cvt_f64_f32_e32 v[108:109], v165
	v_fmac_f64_e32 v[94:95], v[106:107], v[108:109]
	v_cvt_f64_f32_e32 v[106:107], v158
	v_cvt_f64_f32_e32 v[108:109], v166
	v_fmac_f64_e32 v[92:93], v[106:107], v[108:109]
	v_cvt_f64_f32_e32 v[106:107], v159
	v_cvt_f64_f32_e32 v[108:109], v167
	v_fmac_f64_e32 v[94:95], v[106:107], v[108:109]
	s_waitcnt vmcnt(18)
	v_cvt_f64_f32_e32 v[106:107], v176
	s_waitcnt vmcnt(16)
	v_cvt_f64_f32_e32 v[108:109], v184
	v_fmac_f64_e32 v[92:93], v[106:107], v[108:109]
	v_cvt_f64_f32_e32 v[106:107], v177
	v_cvt_f64_f32_e32 v[108:109], v185
	v_fmac_f64_e32 v[94:95], v[106:107], v[108:109]
	v_cvt_f64_f32_e32 v[106:107], v178
	v_cvt_f64_f32_e32 v[108:109], v186
	v_fmac_f64_e32 v[92:93], v[106:107], v[108:109]
	v_cvt_f64_f32_e32 v[106:107], v179
	v_cvt_f64_f32_e32 v[108:109], v187
	v_fmac_f64_e32 v[94:95], v[106:107], v[108:109]
	v_cvt_f64_f32_e32 v[106:107], v172
	v_cvt_f64_f32_e32 v[108:109], v180
	v_fmac_f64_e32 v[92:93], v[106:107], v[108:109]
	v_cvt_f64_f32_e32 v[106:107], v173
	v_cvt_f64_f32_e32 v[108:109], v181
	v_fmac_f64_e32 v[94:95], v[106:107], v[108:109]
	v_cvt_f64_f32_e32 v[106:107], v174
	v_cvt_f64_f32_e32 v[108:109], v182
	v_fmac_f64_e32 v[92:93], v[106:107], v[108:109]
	v_cvt_f64_f32_e32 v[106:107], v175
	v_cvt_f64_f32_e32 v[108:109], v183
	v_fmac_f64_e32 v[94:95], v[106:107], v[108:109]
	s_waitcnt vmcnt(14)
	v_cvt_f64_f32_e32 v[106:107], v192
	s_waitcnt vmcnt(12)
	v_cvt_f64_f32_e32 v[108:109], v200
	v_fmac_f64_e32 v[92:93], v[106:107], v[108:109]
	v_cvt_f64_f32_e32 v[106:107], v193
	v_cvt_f64_f32_e32 v[108:109], v201
	v_fmac_f64_e32 v[94:95], v[106:107], v[108:109]
	v_cvt_f64_f32_e32 v[106:107], v194
	v_cvt_f64_f32_e32 v[108:109], v202
	v_fmac_f64_e32 v[92:93], v[106:107], v[108:109]
	v_cvt_f64_f32_e32 v[106:107], v195
	v_cvt_f64_f32_e32 v[108:109], v203
	v_fmac_f64_e32 v[94:95], v[106:107], v[108:109]
	v_cvt_f64_f32_e32 v[106:107], v188
	v_cvt_f64_f32_e32 v[108:109], v196
	v_fmac_f64_e32 v[92:93], v[106:107], v[108:109]
	v_cvt_f64_f32_e32 v[106:107], v189
	v_cvt_f64_f32_e32 v[108:109], v197
	v_fmac_f64_e32 v[94:95], v[106:107], v[108:109]
	v_cvt_f64_f32_e32 v[106:107], v190
	v_cvt_f64_f32_e32 v[108:109], v198
	v_fmac_f64_e32 v[92:93], v[106:107], v[108:109]
	v_cvt_f64_f32_e32 v[106:107], v191
	v_cvt_f64_f32_e32 v[108:109], v199
	v_fmac_f64_e32 v[94:95], v[106:107], v[108:109]
	s_waitcnt vmcnt(10)
	v_cvt_f64_f32_e32 v[106:107], v204
	s_waitcnt vmcnt(8)
	v_cvt_f64_f32_e32 v[108:109], v208
	v_fmac_f64_e32 v[92:93], v[106:107], v[108:109]
	v_cvt_f64_f32_e32 v[106:107], v205
	v_cvt_f64_f32_e32 v[108:109], v209
	v_fmac_f64_e32 v[94:95], v[106:107], v[108:109]
	v_cvt_f64_f32_e32 v[106:107], v206
	v_cvt_f64_f32_e32 v[108:109], v210
	v_fmac_f64_e32 v[92:93], v[106:107], v[108:109]
	v_cvt_f64_f32_e32 v[106:107], v207
	v_cvt_f64_f32_e32 v[108:109], v211
	v_fmac_f64_e32 v[94:95], v[106:107], v[108:109]
	v_cvt_f64_f32_e32 v[106:107], v74
	v_cvt_f64_f32_e32 v[108:109], v82
	v_cvt_f64_f32_e32 v[74:75], v75
	v_cvt_f64_f32_e32 v[82:83], v83
	v_fmac_f64_e32 v[92:93], v[106:107], v[108:109]
	v_fmac_f64_e32 v[94:95], v[74:75], v[82:83]
	v_cvt_f64_f32_e32 v[74:75], v76
	v_cvt_f64_f32_e32 v[82:83], v84
	v_fmac_f64_e32 v[92:93], v[74:75], v[82:83]
	v_cvt_f64_f32_e32 v[74:75], v77
	v_cvt_f64_f32_e32 v[76:77], v85
	v_fmac_f64_e32 v[94:95], v[74:75], v[76:77]
	s_waitcnt vmcnt(6)
	v_cvt_f64_f32_e32 v[74:75], v66
	s_waitcnt vmcnt(4)
	v_cvt_f64_f32_e32 v[76:77], v78
	v_fmac_f64_e32 v[92:93], v[74:75], v[76:77]
	v_cvt_f64_f32_e32 v[66:67], v67
	v_cvt_f64_f32_e32 v[74:75], v79
	v_fmac_f64_e32 v[94:95], v[66:67], v[74:75]
	v_cvt_f64_f32_e32 v[66:67], v68
	v_cvt_f64_f32_e32 v[74:75], v80
	v_fmac_f64_e32 v[92:93], v[66:67], v[74:75]
	v_cvt_f64_f32_e32 v[66:67], v69
	v_cvt_f64_f32_e32 v[68:69], v81
	v_fmac_f64_e32 v[94:95], v[66:67], v[68:69]
	v_cvt_f64_f32_e32 v[66:67], v54
	v_cvt_f64_f32_e32 v[68:69], v58
	v_cvt_f64_f32_e32 v[54:55], v55
	v_cvt_f64_f32_e32 v[58:59], v59
	v_fmac_f64_e32 v[92:93], v[66:67], v[68:69]
	v_fmac_f64_e32 v[94:95], v[54:55], v[58:59]
	v_cvt_f64_f32_e32 v[54:55], v56
	v_cvt_f64_f32_e32 v[58:59], v60
	v_fmac_f64_e32 v[92:93], v[54:55], v[58:59]
	v_cvt_f64_f32_e32 v[54:55], v57
	v_cvt_f64_f32_e32 v[56:57], v61
	v_fmac_f64_e32 v[94:95], v[54:55], v[56:57]
	s_waitcnt vmcnt(2)
	v_cvt_f64_f32_e32 v[54:55], v62
	s_waitcnt vmcnt(0)
	v_cvt_f64_f32_e32 v[56:57], v120
	v_fmac_f64_e32 v[92:93], v[54:55], v[56:57]
	v_cvt_f64_f32_e32 v[54:55], v63
	v_cvt_f64_f32_e32 v[56:57], v121
	v_fmac_f64_e32 v[94:95], v[54:55], v[56:57]
	v_cvt_f64_f32_e32 v[54:55], v64
	v_cvt_f64_f32_e32 v[56:57], v122
	v_fmac_f64_e32 v[92:93], v[54:55], v[56:57]
	v_cvt_f64_f32_e32 v[54:55], v65
	v_cvt_f64_f32_e32 v[56:57], v123
	v_fmac_f64_e32 v[94:95], v[54:55], v[56:57]
	v_cvt_f64_f32_e32 v[54:55], v50
	v_cvt_f64_f32_e32 v[56:57], v70
	v_fmac_f64_e32 v[92:93], v[54:55], v[56:57]
	v_cvt_f64_f32_e32 v[50:51], v51
	v_cvt_f64_f32_e32 v[54:55], v71
	v_fmac_f64_e32 v[94:95], v[50:51], v[54:55]
	v_cvt_f64_f32_e32 v[50:51], v52
	v_cvt_f64_f32_e32 v[54:55], v72
	v_fmac_f64_e32 v[92:93], v[50:51], v[54:55]
	v_cvt_f64_f32_e32 v[50:51], v53
	v_cvt_f64_f32_e32 v[52:53], v73
	v_fmac_f64_e32 v[94:95], v[50:51], v[52:53]
	v_add_f64 v[50:51], v[92:93], v[94:95]
	s_nop 1
	v_mov_b32_dpp v52, v50 quad_perm:[1,0,3,2] row_mask:0xf bank_mask:0xf
	v_mov_b32_dpp v53, v51 quad_perm:[1,0,3,2] row_mask:0xf bank_mask:0xf
	s_waitcnt lgkmcnt(0)
	v_add_f64 v[50:51], v[50:51], v[52:53]
	s_nop 1
	v_mov_b32_dpp v52, v50 quad_perm:[2,3,0,1] row_mask:0xf bank_mask:0xf
	v_mov_b32_dpp v53, v51 quad_perm:[2,3,0,1] row_mask:0xf bank_mask:0xf
	s_waitcnt lgkmcnt(0)
	v_add_f64 v[50:51], v[50:51], v[52:53]
	s_nop 1
	v_mov_b32_dpp v52, v50 row_half_mirror row_mask:0xf bank_mask:0xf
	v_mov_b32_dpp v53, v51 row_half_mirror row_mask:0xf bank_mask:0xf
	s_waitcnt lgkmcnt(0)
	v_add_f64 v[50:51], v[50:51], v[52:53]
	s_nop 1
	v_mov_b32_dpp v52, v50 row_mirror row_mask:0xf bank_mask:0xf
	v_mov_b32_dpp v53, v51 row_mirror row_mask:0xf bank_mask:0xf
	s_and_saveexec_b64 s[0:1], vcc
	s_cbranch_execz .LBB2_168
	v_lshrrev_b32_e32 v0, 8, v105
	v_lshl_add_u32 v0, v0, 3, 0
	v_lshl_add_u32 v54, v104, 3, 0
	v_add_u32_e32 v0, 0x13450, v0
	v_add_u32_e32 v56, 0x12ed0, v54
	ds_read_b64 v[54:55], v0
	ds_read_b64 v[56:57], v56
	s_waitcnt lgkmcnt(2)
	v_add_f64 v[50:51], v[50:51], v[52:53]
	s_waitcnt lgkmcnt(1)
	v_mul_f64 v[50:51], v[50:51], v[54:55]
	s_waitcnt lgkmcnt(0)
	v_mul_f64 v[50:51], v[50:51], v[56:57]
	ds_write_b64 v101, v[50:51]
	s_branch .LBB2_168

.LBB2_181:
	s_or_b64 exec, exec, s[4:5]
	s_nop 1
	v_mov_b32_dpp v50, v0 quad_perm:[1,0,3,2] row_mask:0xf bank_mask:0xf
	v_mov_b32_dpp v51, v1 quad_perm:[1,0,3,2] row_mask:0xf bank_mask:0xf
	v_mov_b32_dpp v55, v52 quad_perm:[1,0,3,2] row_mask:0xf bank_mask:0xf
	v_mov_b32_e32 v53, v1
	v_mov_b32_e32 v54, v0
	s_waitcnt lgkmcnt(1)
	v_cmp_lt_f64_e64 s[4:5], v[0:1], v[50:51]
	v_cmp_nlt_f64_e64 s[0:1], v[0:1], v[50:51]
	s_and_saveexec_b64 s[6:7], s[0:1]
	s_cbranch_execz .LBB2_183
	v_cmp_eq_f64_e64 s[0:1], v[0:1], v[50:51]
	s_waitcnt lgkmcnt(0)
	v_cmp_lt_i32_e64 s[2:3], v55, v52
	s_and_b64 s[0:1], s[0:1], s[2:3]
	s_andn2_b64 s[2:3], s[4:5], exec
	s_and_b64 s[0:1], s[0:1], exec
	s_or_b64 s[4:5], s[2:3], s[0:1]

.LBB2_185:
	s_or_b64 exec, exec, s[0:1]
	s_nop 1
	v_mov_b32_dpp v50, v54 quad_perm:[2,3,0,1] row_mask:0xf bank_mask:0xf
	v_mov_b32_dpp v51, v53 quad_perm:[2,3,0,1] row_mask:0xf bank_mask:0xf
	s_waitcnt lgkmcnt(2)
	v_mov_b32_dpp v55, v52 quad_perm:[2,3,0,1] row_mask:0xf bank_mask:0xf
	s_waitcnt lgkmcnt(1)
	v_cmp_lt_f64_e64 s[4:5], v[0:1], v[50:51]
	v_cmp_nlt_f64_e64 s[0:1], v[0:1], v[50:51]
	s_and_saveexec_b64 s[6:7], s[0:1]
	s_cbranch_execz .LBB2_187
	v_cmp_eq_f64_e64 s[0:1], v[0:1], v[50:51]
	s_waitcnt lgkmcnt(0)
	v_cmp_lt_i32_e64 s[2:3], v55, v52
	s_and_b64 s[0:1], s[0:1], s[2:3]
	s_andn2_b64 s[2:3], s[4:5], exec
	s_and_b64 s[0:1], s[0:1], exec
	s_or_b64 s[4:5], s[2:3], s[0:1]

.LBB2_189:
	s_or_b64 exec, exec, s[0:1]
	s_nop 1
	v_mov_b32_dpp v50, v54 row_half_mirror row_mask:0xf bank_mask:0xf
	v_mov_b32_dpp v51, v53 row_half_mirror row_mask:0xf bank_mask:0xf
	s_waitcnt lgkmcnt(2)
	v_mov_b32_dpp v55, v52 row_half_mirror row_mask:0xf bank_mask:0xf
	s_waitcnt lgkmcnt(1)
	v_cmp_lt_f64_e64 s[4:5], v[0:1], v[50:51]
	v_cmp_nlt_f64_e64 s[0:1], v[0:1], v[50:51]
	s_and_saveexec_b64 s[6:7], s[0:1]
	s_cbranch_execz .LBB2_191
	v_cmp_eq_f64_e64 s[0:1], v[0:1], v[50:51]
	s_waitcnt lgkmcnt(0)
	v_cmp_lt_i32_e64 s[2:3], v55, v52
	s_and_b64 s[0:1], s[0:1], s[2:3]
	s_andn2_b64 s[2:3], s[4:5], exec
	s_and_b64 s[0:1], s[0:1], exec
	s_or_b64 s[4:5], s[2:3], s[0:1]

.LBB2_193:
	s_or_b64 exec, exec, s[0:1]
	s_nop 1
	v_mov_b32_dpp v50, v54 row_mirror row_mask:0xf bank_mask:0xf
	v_mov_b32_dpp v51, v53 row_mirror row_mask:0xf bank_mask:0xf
	v_mov_b32_dpp v53, v52 row_mirror row_mask:0xf bank_mask:0xf
	s_waitcnt lgkmcnt(1)
	v_cmp_lt_f64_e64 s[4:5], v[0:1], v[50:51]
	v_cmp_nlt_f64_e64 s[0:1], v[0:1], v[50:51]
	s_and_saveexec_b64 s[6:7], s[0:1]
	s_cbranch_execnz .LBB2_198
	s_or_b64 exec, exec, s[6:7]
	s_and_saveexec_b64 s[0:1], s[4:5]
	s_cbranch_execnz .LBB2_199

amdhsa.kernels:
  - .agpr_count:     0
    .args:
      - .actual_access:  read_only
        .address_space:  global
        .offset:         0
        .size:           8
        .value_kind:     global_buffer
      - .actual_access:  read_only
        .address_space:  global
        .offset:         8
        .size:           8
        .value_kind:     global_buffer
      - .actual_access:  write_only
        .address_space:  global
        .offset:         16
        .size:           8
        .value_kind:     global_buffer
      - .actual_access:  write_only
        .address_space:  global
        .offset:         24
        .size:           8
        .value_kind:     global_buffer
      - .actual_access:  write_only
        .address_space:  global
        .offset:         32
        .size:           8
        .value_kind:     global_buffer
      - .actual_access:  write_only
        .address_space:  global
        .offset:         40
        .size:           8
        .value_kind:     global_buffer
      - .actual_access:  write_only
        .address_space:  global
        .offset:         48
        .size:           8
        .value_kind:     global_buffer
      - .actual_access:  write_only
        .address_space:  global
        .offset:         56
        .size:           8
        .value_kind:     global_buffer
      - .actual_access:  write_only
        .address_space:  global
        .offset:         64
        .size:           8
        .value_kind:     global_buffer
    .group_segment_fixed_size: 18944
    .kernarg_segment_align: 8
    .kernarg_segment_size: 72
    .language:       OpenCL C
    .language_version:
      - 2
      - 0
    .max_flat_workgroup_size: 256
    .name:           _Z6k_prepPKfS0_PfS1_PdS2_PtS3_S3_
    .private_segment_fixed_size: 0
    .sgpr_count:     34
    .sgpr_spill_count: 0
    .symbol:         _Z6k_prepPKfS0_PfS1_PdS2_PtS3_S3_.kd
    .uniform_work_group_size: 1
    .uses_dynamic_stack: false
    .vgpr_count:     29
    .vgpr_spill_count: 0
    .wavefront_size: 64
  - .agpr_count:     16
    .args:
      - .actual_access:  read_only
        .address_space:  global
        .offset:         0
        .size:           8
        .value_kind:     global_buffer
      - .actual_access:  read_only
        .address_space:  global
        .offset:         8
        .size:           8
        .value_kind:     global_buffer
      - .actual_access:  read_only
        .address_space:  global
        .offset:         16
        .size:           8
        .value_kind:     global_buffer
      - .actual_access:  read_only
        .address_space:  global
        .offset:         24
        .size:           8
        .value_kind:     global_buffer
      - .actual_access:  write_only
        .address_space:  global
        .offset:         32
        .size:           8
        .value_kind:     global_buffer
    .group_segment_fixed_size: 256
    .kernarg_segment_align: 8
    .kernarg_segment_size: 40
    .language:       OpenCL C
    .language_version:
      - 2
      - 0
    .max_flat_workgroup_size: 256
    .name:           _Z9k_coarse2PKtS0_PKdS2_Pf
    .private_segment_fixed_size: 0
    .sgpr_count:     37
    .sgpr_spill_count: 0
    .symbol:         _Z9k_coarse2PKtS0_PKdS2_Pf.kd
    .uniform_work_group_size: 1
    .uses_dynamic_stack: false
    .vgpr_count:     156
    .vgpr_spill_count: 0
    .wavefront_size: 64
  - .agpr_count:     0
    .args:
      - .actual_access:  read_only
        .address_space:  global
        .offset:         0
        .size:           8
        .value_kind:     global_buffer
      - .actual_access:  read_only
        .address_space:  global
        .offset:         8
        .size:           8
        .value_kind:     global_buffer
      - .actual_access:  read_only
        .address_space:  global
        .offset:         16
        .size:           8
        .value_kind:     global_buffer
      - .actual_access:  read_only
        .address_space:  global
        .offset:         24
        .size:           8
        .value_kind:     global_buffer
      - .actual_access:  read_only
        .address_space:  global
        .offset:         32
        .size:           8
        .value_kind:     global_buffer
      - .actual_access:  read_only
        .address_space:  global
        .offset:         40
        .size:           8
        .value_kind:     global_buffer
      - .actual_access:  read_only
        .address_space:  global
        .offset:         48
        .size:           8
        .value_kind:     global_buffer
      - .actual_access:  write_only
        .address_space:  global
        .offset:         56
        .size:           8
        .value_kind:     global_buffer
      - .actual_access:  write_only
        .address_space:  global
        .offset:         64
        .size:           8
        .value_kind:     global_buffer
      - .actual_access:  write_only
        .address_space:  global
        .offset:         72
        .size:           8
        .value_kind:     global_buffer
      - .actual_access:  read_only
        .address_space:  global
        .offset:         80
        .size:           8
        .value_kind:     global_buffer
      - .actual_access:  read_only
        .address_space:  global
        .offset:         88
        .size:           8
        .value_kind:     global_buffer
      - .actual_access:  write_only
        .address_space:  global
        .offset:         96
        .size:           8
        .value_kind:     global_buffer
      - .actual_access:  write_only
        .address_space:  global
        .offset:         104
        .size:           8
        .value_kind:     global_buffer
    .group_segment_fixed_size: 0
    .kernarg_segment_align: 8
    .kernarg_segment_size: 112
    .language:       OpenCL C
    .language_version:
      - 2
      - 0
    .max_flat_workgroup_size: 512
    .name:           _Z7k_fine3PKfS0_PKtS2_PKdS4_S0_PiPfS5_S0_S0_PtS7_
    .private_segment_fixed_size: 0
    .sgpr_count:     106
    .sgpr_spill_count: 4
    .symbol:         _Z7k_fine3PKfS0_PKtS2_PKdS4_S0_PiPfS5_S0_S0_PtS7_.kd
    .uniform_work_group_size: 1
    .uses_dynamic_stack: false
    .vgpr_count:     229
    .vgpr_spill_count: 0
    .wavefront_size: 64
  - .agpr_count:     0
    .args:
      - .actual_access:  read_only
        .address_space:  global
        .offset:         0
        .size:           8
        .value_kind:     global_buffer
      - .actual_access:  read_only
        .address_space:  global
        .offset:         8
        .size:           8
        .value_kind:     global_buffer
      - .actual_access:  read_only
        .address_space:  global
        .offset:         16
        .size:           8
        .value_kind:     global_buffer
      - .actual_access:  read_only
        .address_space:  global
        .offset:         24
        .size:           8
        .value_kind:     global_buffer
      - .actual_access:  read_only
        .address_space:  global
        .offset:         32
        .size:           8
        .value_kind:     global_buffer
      - .actual_access:  read_only
        .address_space:  global
        .offset:         40
        .size:           8
        .value_kind:     global_buffer
      - .actual_access:  write_only
        .address_space:  global
        .offset:         48
        .size:           8
        .value_kind:     global_buffer
      - .actual_access:  write_only
        .address_space:  global
        .offset:         56
        .size:           8
        .value_kind:     global_buffer
      - .actual_access:  write_only
        .address_space:  global
        .offset:         64
        .size:           8
        .value_kind:     global_buffer
    .group_segment_fixed_size: 18512
    .kernarg_segment_align: 8
    .kernarg_segment_size: 72
    .language:       OpenCL C
    .language_version:
      - 2
      - 0
    .max_flat_workgroup_size: 256
    .name:           _Z10k_transferPKtS0_PKfPKiS2_S4_PfS5_S5_
    .private_segment_fixed_size: 0
    .sgpr_count:     34
    .sgpr_spill_count: 0
    .symbol:         _Z10k_transferPKtS0_PKfPKiS2_S4_PfS5_S5_.kd
    .uniform_work_group_size: 1
    .uses_dynamic_stack: false
    .vgpr_count:     49
    .vgpr_spill_count: 0
    .wavefront_size: 64
